# gdnprep conv: k / v segment rows loaded together with the q rows into spare registers (one load latency per unit instead of three)
# baseline (speedup 1.0000x reference)
; DI void gdn_prep_unit(const Params& p, int U, char* lds) {
;     ...
;     for (int X = 0; X < 3; ++X) {
;       const int col = 1536 + 512 * X + h * 128 + 2 * lane, cb = 512 * X + h * 128 + 2 * lane;
;       float w0[4], w1[4];
; #pragma unroll
;       for (int j = 0; j < 4; ++j) { w0[j] = p.conv_w[j * 1536 + cb]; w1[j] = p.conv_w[j * 1536 + cb + 1]; }
;       bf16_t* dst = X == 0 ? q_s : (X == 1 ? k_s : v_s);
;       const int i0 = 16 * wid;
;       unsigned raw[19];
;       {
;         const unsigned* pr[19];
; #pragma unroll
;         for (int j = 0; j < 19; ++j) { const int rr = i0 - 3 + j; const int rc = (s0 + rr >= 0) ? rr : -s0;
;           pr[j] = (const unsigned*)(proj + (size_t)((long)t0 + rc) * PP + col); }
;         asm volatile("global_load_dword %0, %10, off\n\tglobal_load_dword %1, %11, off\n\tglobal_load_dword %2, %12, off\n\tglobal_load_dword %3, %13, off\n\tglobal_load_dword %4, %14, off\n\t"
;                      "global_load_dword %5, %15, off\n\tglobal_load_dword %6, %16, off\n\tglobal_load_dword %7, %17, off\n\tglobal_load_dword %8, %18, off\n\tglobal_load_dword %9, %19, off\n\ts_waitcnt vmcnt(0)"
;                      : "=&v"(raw[0]), "=&v"(raw[1]), "=&v"(raw[2]), "=&v"(raw[3]), "=&v"(raw[4]), "=&v"(raw[5]), "=&v"(raw[6]), "=&v"(raw[7]), "=&v"(raw[8]), "=&v"(raw[9])
;                      : "v"(pr[0]), "v"(pr[1]), "v"(pr[2]), "v"(pr[3]), "v"(pr[4]), "v"(pr[5]), "v"(pr[6]), "v"(pr[7]), "v"(pr[8]), "v"(pr[9]) : "memory");
;         asm volatile("global_load_dword %0, %9, off\n\tglobal_load_dword %1, %10, off\n\tglobal_load_dword %2, %11, off\n\tglobal_load_dword %3, %12, off\n\tglobal_load_dword %4, %13, off\n\t"
;                      "global_load_dword %5, %14, off\n\tglobal_load_dword %6, %15, off\n\tglobal_load_dword %7, %16, off\n\tglobal_load_dword %8, %17, off\n\ts_waitcnt vmcnt(0)"
;                      : "=&v"(raw[10]), "=&v"(raw[11]), "=&v"(raw[12]), "=&v"(raw[13]), "=&v"(raw[14]), "=&v"(raw[15]), "=&v"(raw[16]), "=&v"(raw[17]), "=&v"(raw[18])
;                      : "v"(pr[10]), "v"(pr[11]), "v"(pr[12]), "v"(pr[13]), "v"(pr[14]), "v"(pr[15]), "v"(pr[16]), "v"(pr[17]), "v"(pr[18]) : "memory");
.LBB0_1092:
	s_or_b64 exec, exec, s[8:9]
	v_ashrrev_i32_e32 v181, 6, v175
	v_lshlrev_b32_e32 v27, 4, v181
	v_sub_u32_e32 v62, 0, v3
	v_or_b32_e32 v180, 6, v27
	v_add_u32_e32 v84, v27, v3
	v_lshlrev_b32_e32 v3, 4, v175
	v_max_i32_e32 v42, v180, v62
	v_lshrrev_b32_e32 v31, 4, v178
	v_lshlrev_b64 v[4:5], 14, v[34:35]
	v_and_b32_e32 v85, 32, v3
	v_lshrrev_b32_e32 v3, 5, v175
	s_mov_b32 s0, 0x1fffffc
	v_lshlrev_b32_e32 v6, 3, v175
	v_ashrrev_i32_e32 v43, 31, v42
	v_lshl_add_u64 v[66:67], s[66:67], 0, v[4:5]
	v_lshlrev_b32_e32 v4, 1, v178
	v_and_or_b32 v3, v3, s0, v31
	v_and_b32_e32 v6, 64, v6
	v_lshl_add_u64 v[42:43], v[0:1], 0, v[42:43]
	v_lshl_or_b32 v2, v2, 7, v4
	v_add_u32_e32 v5, -3, v27
	v_and_b32_e32 v99, 4, v175
	v_lshl_or_b32 v87, v3, 7, v6
	v_add_u32_e32 v6, -2, v27
	v_add_u32_e32 v8, -1, v27
	v_or_b32_e32 v190, 1, v27
	v_or_b32_e32 v187, 2, v27
	v_or_b32_e32 v185, 3, v27
	v_or_b32_e32 v183, 4, v27
	v_or_b32_e32 v182, 5, v27
	v_mul_lo_u32 v194, v43, s3
	v_or_b32_e32 v43, 7, v27
	v_and_or_b32 v93, v4, 2, v99
	v_lshlrev_b32_e32 v70, 2, v2
	v_lshlrev_b32_e32 v2, 1, v2
	v_mov_b32_e32 v3, v30
	v_max_i32_e32 v4, v5, v62
	v_max_i32_e32 v6, v6, v62
	v_max_i32_e32 v8, v8, v62
	v_max_i32_e32 v18, v27, v62
	v_max_i32_e32 v20, v190, v62
	v_max_i32_e32 v22, v187, v62
	v_max_i32_e32 v24, v185, v62
	v_max_i32_e32 v38, v183, v62
	v_max_i32_e32 v40, v182, v62
	v_max_i32_e32 v44, v43, v62
	v_lshl_add_u64 v[10:11], s[58:59], 0, v[2:3]
	s_mov_b64 s[0:1], 0xc00
	v_ashrrev_i32_e32 v5, 31, v4
	v_ashrrev_i32_e32 v7, 31, v6
	v_ashrrev_i32_e32 v9, 31, v8
	v_ashrrev_i32_e32 v19, 31, v18
	v_ashrrev_i32_e32 v21, 31, v20
	v_ashrrev_i32_e32 v23, 31, v22
	v_ashrrev_i32_e32 v25, 31, v24
	v_ashrrev_i32_e32 v39, 31, v38
	v_ashrrev_i32_e32 v41, 31, v40
	v_ashrrev_i32_e32 v45, 31, v44
	v_lshl_add_u64 v[2:3], v[10:11], 0, s[0:1]
	v_lshl_add_u64 v[12:13], v[0:1], 0, v[4:5]
	v_lshl_add_u64 v[14:15], v[0:1], 0, v[6:7]
	v_lshl_add_u64 v[16:17], v[0:1], 0, v[8:9]
	v_lshl_add_u64 v[18:19], v[0:1], 0, v[18:19]
	v_lshl_add_u64 v[20:21], v[0:1], 0, v[20:21]
	v_lshl_add_u64 v[22:23], v[0:1], 0, v[22:23]
	v_lshl_add_u64 v[24:25], v[0:1], 0, v[24:25]
	v_lshl_add_u64 v[38:39], v[0:1], 0, v[38:39]
	v_lshl_add_u64 v[40:41], v[0:1], 0, v[40:41]
	v_lshl_add_u64 v[44:45], v[0:1], 0, v[44:45]
	v_mov_b32_e32 v71, v30
	v_mad_u64_u32 v[4:5], s[0:1], v12, s3, v[2:3]
	v_mad_u64_u32 v[6:7], s[0:1], v14, s3, v[2:3]
	v_mad_u64_u32 v[8:9], s[0:1], v16, s3, v[2:3]
	v_mad_u64_u32 v[36:37], s[0:1], v18, s3, v[2:3]
	v_mad_u64_u32 v[72:73], s[0:1], v20, s3, v[2:3]
	v_mad_u64_u32 v[82:83], s[0:1], v22, s3, v[2:3]
	v_mad_u64_u32 v[88:89], s[0:1], v24, s3, v[2:3]
	v_mad_u64_u32 v[90:91], s[0:1], v38, s3, v[2:3]
	v_mad_u64_u32 v[94:95], s[0:1], v40, s3, v[2:3]
	v_mad_u64_u32 v[96:97], s[0:1], v42, s3, v[2:3]
	v_mad_u64_u32 v[100:101], s[0:1], v44, s3, v[2:3]
	v_lshl_add_u64 v[68:69], s[70:71], 0, v[70:71]
	s_movk_i32 s0, 0x1000
	v_add_co_u32_e32 v64, vcc, s0, v68
	s_movk_i32 s0, 0x4000
	s_nop 0
	v_addc_co_u32_e32 v65, vcc, 0, v69, vcc
	v_add_co_u32_e32 v56, vcc, s0, v68
	s_waitcnt lgkmcnt(0)
	s_barrier
	v_addc_co_u32_e32 v57, vcc, 0, v69, vcc
	global_load_dwordx2 v[74:75], v70, s[70:71]
	global_load_dwordx2 v[76:77], v[56:57], off offset:-4096
	global_load_dwordx2 v[78:79], v[56:57], off offset:2048
	global_load_dwordx2 v[80:81], v[64:65], off offset:2048
	v_or_b32_e32 v192, 8, v27
	v_or_b32_e32 v191, 9, v27
	v_or_b32_e32 v186, 10, v27
	v_max_i32_e32 v46, v192, v62
	v_max_i32_e32 v48, v191, v62
	v_max_i32_e32 v50, v186, v62
	v_ashrrev_i32_e32 v47, 31, v46
	v_ashrrev_i32_e32 v49, 31, v48
	v_ashrrev_i32_e32 v51, 31, v50
	v_lshl_add_u64 v[46:47], v[0:1], 0, v[46:47]
	v_lshl_add_u64 v[48:49], v[0:1], 0, v[48:49]
	v_lshl_add_u64 v[50:51], v[0:1], 0, v[50:51]
	v_mul_lo_u32 v193, v41, s3
	v_mul_lo_u32 v195, v47, s3
	v_mul_lo_u32 v196, v49, s3
	v_mul_lo_u32 v197, v51, s3
	v_or_b32_e32 v184, 11, v27
	v_or_b32_e32 v51, 12, v27
	v_or_b32_e32 v49, 13, v27
	v_or_b32_e32 v47, 14, v27
	v_or_b32_e32 v41, 15, v27
	v_max_i32_e32 v52, v184, v62
	v_max_i32_e32 v54, v51, v62
	v_max_i32_e32 v58, v49, v62
	v_max_i32_e32 v60, v47, v62
	v_max_i32_e32 v62, v41, v62
	v_mul_lo_u32 v13, v13, s3
	v_ashrrev_i32_e32 v53, 31, v52
	v_ashrrev_i32_e32 v55, 31, v54
	v_ashrrev_i32_e32 v59, 31, v58
	v_ashrrev_i32_e32 v61, 31, v60
	v_ashrrev_i32_e32 v63, 31, v62
	v_add_u32_e32 v5, v13, v5
	v_mul_lo_u32 v15, v15, s3
	v_mul_lo_u32 v17, v17, s3
	v_mul_lo_u32 v19, v19, s3
	v_mul_lo_u32 v21, v21, s3
	v_mul_lo_u32 v23, v23, s3
	v_mul_lo_u32 v25, v25, s3
	v_mul_lo_u32 v39, v39, s3
	v_lshl_add_u64 v[52:53], v[0:1], 0, v[52:53]
	v_lshl_add_u64 v[54:55], v[0:1], 0, v[54:55]
	v_lshl_add_u64 v[58:59], v[0:1], 0, v[58:59]
	v_lshl_add_u64 v[60:61], v[0:1], 0, v[60:61]
	v_lshl_add_u64 v[62:63], v[0:1], 0, v[62:63]
	v_cmp_gt_i32_e64 s[8:9], 2, v84
	v_add_u32_e32 v7, v15, v7
	v_add_u32_e32 v9, v17, v9
	v_add_u32_e32 v37, v19, v37
	v_add_u32_e32 v73, v21, v73
	v_add_u32_e32 v83, v23, v83
	v_add_u32_e32 v89, v25, v89
	v_add_u32_e32 v91, v39, v91
	v_add_u32_e32 v95, v193, v95
	v_add_u32_e32 v97, v194, v97
	v_mad_u64_u32 v[102:103], s[0:1], v46, s3, v[2:3]
	v_mad_u64_u32 v[106:107], s[0:1], v48, s3, v[2:3]
	v_mad_u64_u32 v[108:109], s[0:1], v50, s3, v[2:3]
	v_mad_u64_u32 v[112:113], s[0:1], v52, s3, v[2:3]
	v_mul_lo_u32 v198, v53, s3
	v_mad_u64_u32 v[114:115], s[0:1], v54, s3, v[2:3]
	v_mul_lo_u32 v199, v55, s3
	v_mad_u64_u32 v[118:119], s[0:1], v58, s3, v[2:3]
	v_mad_u64_u32 v[120:121], s[0:1], v60, s3, v[2:3]
	v_mad_u64_u32 v[0:1], s[0:1], v62, s3, v[2:3]
	global_load_dword v2, v[4:5], off
	global_load_dword v3, v[6:7], off
	global_load_dword v53, v[8:9], off
	global_load_dword v55, v[36:37], off
	global_load_dword v86, v[72:73], off
	global_load_dword v92, v[82:83], off
	global_load_dword v98, v[88:89], off
	global_load_dword v104, v[90:91], off
	global_load_dword v110, v[94:95], off
	global_load_dword v116, v[96:97], off
	global_load_dword v212, v[4:5], off offset:1024
	global_load_dword v231, v[4:5], off offset:2048
	global_load_dword v213, v[6:7], off offset:1024
	global_load_dword v232, v[6:7], off offset:2048
	global_load_dword v214, v[8:9], off offset:1024
	global_load_dword v233, v[8:9], off offset:2048
	global_load_dword v215, v[36:37], off offset:1024
	global_load_dword v234, v[36:37], off offset:2048
	global_load_dword v216, v[72:73], off offset:1024
	global_load_dword v235, v[72:73], off offset:2048
	global_load_dword v217, v[82:83], off offset:1024
	global_load_dword v236, v[82:83], off offset:2048
	global_load_dword v218, v[88:89], off offset:1024
	global_load_dword v237, v[88:89], off offset:2048
	global_load_dword v219, v[90:91], off offset:1024
	global_load_dword v238, v[90:91], off offset:2048
	global_load_dword v220, v[94:95], off offset:1024
	global_load_dword v239, v[94:95], off offset:2048
	global_load_dword v221, v[96:97], off offset:1024
	global_load_dword v240, v[96:97], off offset:2048
	s_waitcnt vmcnt(0)
; DI float bflo(unsigned u) { return __uint_as_float(u << 16); }
; DI float bfhi(unsigned u) { return __uint_as_float(u & 0xffff0000u); }
; DI float sigmoidf_(float x) { return __builtin_amdgcn_rcpf(1.f + __expf(-x)); }
; DI void gdn_prep_unit(const Params& p, int U, char* lds) {
;     ...
;         asm volatile("global_load_dword %0, %9, off\n\tglobal_load_dword %1, %10, off\n\tglobal_load_dword %2, %11, off\n\tglobal_load_dword %3, %12, off\n\tglobal_load_dword %4, %13, off\n\t"
;                      "global_load_dword %5, %14, off\n\tglobal_load_dword %6, %15, off\n\tglobal_load_dword %7, %16, off\n\tglobal_load_dword %8, %17, off\n\ts_waitcnt vmcnt(0)"
;                      : "=&v"(raw[10]), "=&v"(raw[11]), "=&v"(raw[12]), "=&v"(raw[13]), "=&v"(raw[14]), "=&v"(raw[15]), "=&v"(raw[16]), "=&v"(raw[17]), "=&v"(raw[18])
;                      : "v"(pr[10]), "v"(pr[11]), "v"(pr[12]), "v"(pr[13]), "v"(pr[14]), "v"(pr[15]), "v"(pr[16]), "v"(pr[17]), "v"(pr[18]) : "memory");
; #pragma unroll
;         for (int j = 0; j < 3; ++j) if (s0 + i0 - 3 + j < 0) raw[j] = 0u;
;       }
;       float y0[16], y1[16], ssr[16];
; #pragma unroll
;       for (int ii = 0; ii < 16; ++ii) {
;         float a0 = w0[0] * bflo(raw[ii]) + w0[1] * bflo(raw[ii + 1]) + w0[2] * bflo(raw[ii + 2]) + w0[3] * bflo(raw[ii + 3]);
;         float a1 = w1[0] * bfhi(raw[ii]) + w1[1] * bfhi(raw[ii + 1]) + w1[2] * bfhi(raw[ii + 2]) + w1[3] * bfhi(raw[ii + 3]);
;         a0 = a0 * sigmoidf_(a0); a1 = a1 * sigmoidf_(a1);
;         y0[ii] = a0; y1[ii] = a1; ssr[ii] = a0 * a0 + a1 * a1;
;       }
	v_cmp_gt_i32_e32 vcc, 3, v84
	v_cndmask_b32_e64 v5, v3, 0, s[8:9]
	v_cmp_gt_i32_e64 s[10:11], 1, v84
	v_cndmask_b32_e64 v4, v2, 0, vcc
	v_lshlrev_b32_e32 v6, 16, v5
	v_and_b32_e32 v7, 0xffff0000, v5
	v_cndmask_b32_e64 v8, v53, 0, s[10:11]
	v_lshlrev_b32_e32 v2, 16, v4
	v_and_b32_e32 v3, 0xffff0000, v4
	s_waitcnt vmcnt(0)
	v_pk_mul_f32 v[4:5], v[80:81], v[6:7]
	v_lshlrev_b32_e32 v94, 16, v8
	v_pk_fma_f32 v[2:3], v[74:75], v[2:3], v[4:5]
	v_and_b32_e32 v95, 0xffff0000, v8
	v_pk_fma_f32 v[2:3], v[76:77], v[94:95], v[2:3]
	v_lshlrev_b32_e32 v124, 16, v55
	v_and_b32_e32 v125, 0xffff0000, v55
	v_pk_fma_f32 v[2:3], v[78:79], v[124:125], v[2:3]
	s_movk_i32 s0, 0x3000
	v_mul_f32_e32 v4, 0xbfb8aa3b, v2
	v_mul_f32_e32 v5, 0xbfb8aa3b, v3
	v_exp_f32_e32 v4, v4
	v_exp_f32_e32 v5, v5
	v_add_co_u32_e64 v72, s[0:1], s0, v68
	v_add_f32_e32 v4, 1.0, v4
	v_add_f32_e32 v5, 1.0, v5
	v_rcp_f32_e32 v4, v4
	v_rcp_f32_e32 v5, v5
	v_mul_lo_u32 v45, v45, s3
	v_mul_lo_u32 v59, v59, s3
	v_mul_lo_u32 v61, v61, s3
	v_mul_lo_u32 v63, v63, s3
	v_addc_co_u32_e64 v73, s[0:1], 0, v69, s[0:1]
	v_pk_mul_f32 v[82:83], v[2:3], v[4:5]
	v_pk_mul_f32 v[88:89], v[80:81], v[94:95]
	v_add_u32_e32 v101, v45, v101
	v_add_u32_e32 v103, v195, v103
	v_add_u32_e32 v107, v196, v107
	v_add_u32_e32 v109, v197, v109
	v_add_u32_e32 v113, v198, v113
	v_add_u32_e32 v115, v199, v115
	v_add_u32_e32 v119, v59, v119
	v_add_u32_e32 v121, v61, v121
	v_add_u32_e32 v1, v63, v1
	global_load_dword v122, v[100:101], off
	global_load_dword v153, v[102:103], off
	global_load_dword v154, v[106:107], off
	global_load_dword v156, v[108:109], off
	global_load_dword v159, v[112:113], off
	global_load_dword v158, v[114:115], off
	global_load_dword v160, v[118:119], off
	global_load_dword v162, v[120:121], off
	global_load_dword v71, v[0:1], off
	global_load_dword v222, v[100:101], off offset:1024
	global_load_dword v241, v[100:101], off offset:2048
	global_load_dword v223, v[102:103], off offset:1024
	global_load_dword v242, v[102:103], off offset:2048
	global_load_dword v224, v[106:107], off offset:1024
	global_load_dword v243, v[106:107], off offset:2048
	global_load_dword v225, v[108:109], off offset:1024
	global_load_dword v244, v[108:109], off offset:2048
	global_load_dword v226, v[112:113], off offset:1024
	global_load_dword v245, v[112:113], off offset:2048
	global_load_dword v227, v[114:115], off offset:1024
	global_load_dword v246, v[114:115], off offset:2048
	global_load_dword v228, v[118:119], off offset:1024
	global_load_dword v247, v[118:119], off offset:2048
	global_load_dword v229, v[120:121], off offset:1024
	global_load_dword v248, v[120:121], off offset:2048
	global_load_dword v230, v[0:1], off offset:1024
	global_load_dword v249, v[0:1], off offset:2048
	s_waitcnt vmcnt(0)
	v_mul_f32_e32 v0, v83, v83
	v_cmp_lt_i32_e64 s[0:1], v164, v166
	v_pk_fma_f32 v[6:7], v[74:75], v[6:7], v[88:89]
	v_pk_fma_f32 v[4:5], v[82:83], v[82:83], v[0:1] op_sel_hi:[1,1,0]
	v_cndmask_b32_e64 v0, v123, v164, s[0:1]
	v_and_b32_e32 v53, 0xffffffc0, v175
	v_pk_fma_f32 v[6:7], v[76:77], v[124:125], v[6:7]
	v_lshlrev_b32_e32 v106, 16, v86
	v_and_b32_e32 v107, 0xffff0000, v86
	v_lshl_add_u32 v36, v178, 2, v146
	v_lshlrev_b32_e32 v55, 2, v0
	v_add_u32_e32 v0, v29, v53
	s_movk_i32 s0, 0x1100
	v_lshl_add_u32 v5, v183, 2, v29
	v_pk_fma_f32 v[6:7], v[78:79], v[106:107], v[6:7]
	ds_read_b128 v[0:3], v0 offset:512
	ds_read_b128 v[126:129], v5 offset:512
	v_mad_u64_u32 v[8:9], s[0:1], v181, s0, v[36:37]
	v_mul_f32_e32 v5, 0xbfb8aa3b, v6
	v_exp_f32_e32 v5, v5
	v_mul_f32_e32 v9, 0xbfb8aa3b, v7
	v_exp_f32_e32 v9, v9
	s_waitcnt lgkmcnt(1)
	v_mul_f32_e32 v84, 0x3db504f3, v0
	v_add_f32_e32 v5, 1.0, v5
	v_rcp_f32_e32 v88, v5
	v_add_f32_e32 v5, 1.0, v9
	v_rcp_f32_e32 v89, v5
	v_and_b32_e32 v0, 16, v27
	v_or3_b32 v0, v85, v0, v87
	v_lshl_or_b32 v90, v0, 3, v93
	v_pk_mul_f32 v[88:89], v[6:7], v[88:89]
	v_mul_f32_e32 v86, 0x3db504f3, v1
	v_mul_f32_e32 v0, v89, v89
	v_pk_fma_f32 v[138:139], v[88:89], v[88:89], v[0:1] op_sel_hi:[1,1,0]
	v_pk_mul_f32 v[0:1], v[80:81], v[124:125]
	v_lshlrev_b32_e32 v6, 16, v92
	v_pk_fma_f32 v[0:1], v[74:75], v[94:95], v[0:1]
	v_and_b32_e32 v7, 0xffff0000, v92
	v_pk_fma_f32 v[0:1], v[76:77], v[106:107], v[0:1]
	v_mad_u64_u32 v[36:37], s[0:1], v190, s18, v[36:37]
	v_pk_fma_f32 v[0:1], v[78:79], v[6:7], v[0:1]
	v_pk_mul_f32 v[100:101], v[80:81], v[106:107]
	v_mul_f32_e32 v9, 0xbfb8aa3b, v0
	v_exp_f32_e32 v9, v9
	v_mul_f32_e32 v37, 0xbfb8aa3b, v1
	v_exp_f32_e32 v37, v37
	v_pk_fma_f32 v[100:101], v[74:75], v[124:125], v[100:101]
	v_add_f32_e32 v9, 1.0, v9
	v_rcp_f32_e32 v94, v9
	v_add_f32_e32 v9, 1.0, v37
	v_rcp_f32_e32 v95, v9
	v_bitop3_b32 v5, v27, 17, 1 bitop3:0xc8
	v_pk_fma_f32 v[100:101], v[76:77], v[6:7], v[100:101]
	v_or3_b32 v5, v85, v5, v87
	v_pk_mul_f32 v[94:95], v[0:1], v[94:95]
	v_lshl_or_b32 v96, v5, 3, v93
	v_mul_f32_e32 v0, v95, v95
	v_pk_fma_f32 v[136:137], v[94:95], v[94:95], v[0:1] op_sel_hi:[1,1,0]
	v_lshlrev_b32_e32 v0, 16, v98
	v_and_b32_e32 v1, 0xffff0000, v98
	v_pk_fma_f32 v[100:101], v[78:79], v[0:1], v[100:101]
	v_mul_f32_e32 v92, 0x3db504f3, v2
	v_mul_f32_e32 v5, 0xbfb8aa3b, v100
	v_exp_f32_e32 v5, v5
	v_mul_f32_e32 v9, 0xbfb8aa3b, v101
	v_exp_f32_e32 v9, v9
	v_bitop3_b32 v2, v27, 18, 2 bitop3:0xc8
	v_add_f32_e32 v5, 1.0, v5
	v_rcp_f32_e32 v108, v5
	v_add_f32_e32 v5, 1.0, v9
	v_rcp_f32_e32 v109, v5
	v_or3_b32 v2, v85, v2, v87
	v_lshl_or_b32 v102, v2, 3, v93
	v_mul_f32_e32 v98, 0x3db504f3, v3
	v_pk_mul_f32 v[100:101], v[100:101], v[108:109]
	v_pk_mul_f32 v[108:109], v[80:81], v[6:7]
	v_mul_f32_e32 v2, v101, v101
	v_pk_fma_f32 v[106:107], v[74:75], v[106:107], v[108:109]
	v_pk_fma_f32 v[134:135], v[100:101], v[100:101], v[2:3] op_sel_hi:[1,1,0]
	v_lshlrev_b32_e32 v2, 16, v104
	v_and_b32_e32 v3, 0xffff0000, v104
	v_pk_fma_f32 v[106:107], v[76:77], v[0:1], v[106:107]
	v_lshlrev_b32_e32 v130, 16, v110
	v_pk_fma_f32 v[106:107], v[78:79], v[2:3], v[106:107]
	v_and_b32_e32 v131, 0xffff0000, v110
	v_mul_f32_e32 v9, 0xbfb8aa3b, v106
	v_exp_f32_e32 v9, v9
	v_mul_f32_e32 v37, 0xbfb8aa3b, v107
	v_exp_f32_e32 v37, v37
	v_lshlrev_b32_e32 v148, 16, v116
	v_add_f32_e32 v9, 1.0, v9
	v_rcp_f32_e32 v112, v9
	v_add_f32_e32 v9, 1.0, v37
	v_rcp_f32_e32 v113, v9
	v_and_b32_e32 v149, 0xffff0000, v116
	v_lshlrev_b32_e32 v150, 16, v122
	v_and_b32_e32 v151, 0xffff0000, v122
	v_pk_mul_f32 v[106:107], v[106:107], v[112:113]
	v_pk_mul_f32 v[112:113], v[80:81], v[0:1]
	v_mul_f32_e32 v104, v107, v107
	v_pk_fma_f32 v[6:7], v[74:75], v[6:7], v[112:113]
	v_pk_fma_f32 v[132:133], v[106:107], v[106:107], v[104:105] op_sel_hi:[1,1,0]
	v_pk_fma_f32 v[6:7], v[76:77], v[2:3], v[6:7]
	s_waitcnt lgkmcnt(0)
; DI float bflo(unsigned u) { return __uint_as_float(u << 16); }
; DI float bfhi(unsigned u) { return __uint_as_float(u & 0xffff0000u); }
; DI float swap32sum(float a, float b) { const auto r = __builtin_amdgcn_permlane32_swap(__float_as_uint(a), __float_as_uint(b), false, false); return __uint_as_float(r[0]) + __uint_as_float(r[1]); }
; DI float sigmoidf_(float x) { return __builtin_amdgcn_rcpf(1.f + __expf(-x)); }
; DI void gdn_prep_unit(const Params& p, int U, char* lds) {
;     ...
; #pragma unroll
;       for (int ii = 0; ii < 16; ++ii) {
;         float a0 = w0[0] * bflo(raw[ii]) + w0[1] * bflo(raw[ii + 1]) + w0[2] * bflo(raw[ii + 2]) + w0[3] * bflo(raw[ii + 3]);
;         float a1 = w1[0] * bfhi(raw[ii]) + w1[1] * bfhi(raw[ii + 1]) + w1[2] * bfhi(raw[ii + 2]) + w1[3] * bfhi(raw[ii + 3]);
;         a0 = a0 * sigmoidf_(a0); a1 = a1 * sigmoidf_(a1);
;         y0[ii] = a0; y1[ii] = a1; ssr[ii] = a0 * a0 + a1 * a1;
;       }
;       if (X < 2) {
;         const bool b3 = (lane & 8) != 0, b2 = (lane & 4) != 0;
;         float r8[8], r4[4], r2[2];
; #pragma unroll
;         for (int j = 0; j < 8; ++j) r8[j] = swap32sum(ssr[j], ssr[8 + j]);
	v_mul_f32_e32 v104, 0x3db504f3, v126
	v_pk_fma_f32 v[6:7], v[78:79], v[130:131], v[6:7]
	v_mul_f32_e32 v110, 0x3db504f3, v127
	v_mul_f32_e32 v9, 0xbfb8aa3b, v6
	v_exp_f32_e32 v9, v9
	v_mul_f32_e32 v37, 0xbfb8aa3b, v7
	v_exp_f32_e32 v37, v37
	v_lshlrev_b32_e32 v202, 16, v154
	v_add_f32_e32 v9, 1.0, v9
	v_rcp_f32_e32 v114, v9
	v_add_f32_e32 v9, 1.0, v37
	v_rcp_f32_e32 v115, v9
	v_and_b32_e32 v203, 0xffff0000, v154
	v_pk_mul_f32 v[154:155], v[80:81], v[150:151]
	v_lshlrev_b32_e32 v152, 16, v153
	v_pk_mul_f32 v[114:115], v[6:7], v[114:115]
	v_and_b32_e32 v153, 0xffff0000, v153
	v_mul_f32_e32 v6, v115, v115
	v_pk_fma_f32 v[140:141], v[114:115], v[114:115], v[6:7] op_sel_hi:[1,1,0]
	v_pk_mul_f32 v[6:7], v[80:81], v[2:3]
	v_bitop3_b32 v5, v27, 19, 3 bitop3:0xc8
	v_pk_fma_f32 v[0:1], v[74:75], v[0:1], v[6:7]
	v_or3_b32 v5, v85, v5, v87
	v_pk_fma_f32 v[0:1], v[76:77], v[130:131], v[0:1]
	v_lshl_or_b32 v108, v5, 3, v93
	v_pk_fma_f32 v[0:1], v[78:79], v[148:149], v[0:1]
	v_bitop3_b32 v5, v27, 20, 4 bitop3:0xc8
	v_mul_f32_e32 v6, 0xbfb8aa3b, v0
	v_mul_f32_e32 v7, 0xbfb8aa3b, v1
	v_exp_f32_e32 v6, v6
	v_exp_f32_e32 v7, v7
	v_or3_b32 v5, v85, v5, v87
	v_lshl_or_b32 v112, v5, 3, v93
	v_add_f32_e32 v6, 1.0, v6
	v_add_f32_e32 v7, 1.0, v7
	v_rcp_f32_e32 v6, v6
	v_rcp_f32_e32 v7, v7
	v_bitop3_b32 v5, v27, 21, 5 bitop3:0xc8
	v_or3_b32 v5, v85, v5, v87
	v_lshl_or_b32 v118, v5, 3, v93
	v_pk_mul_f32 v[120:121], v[0:1], v[6:7]
	v_bitop3_b32 v5, v27, 22, 6 bitop3:0xc8
	v_mul_f32_e32 v0, v121, v121
	v_pk_fma_f32 v[142:143], v[120:121], v[120:121], v[0:1] op_sel_hi:[1,1,0]
	v_pk_mul_f32 v[0:1], v[80:81], v[130:131]
	v_or3_b32 v5, v85, v5, v87
	v_pk_fma_f32 v[0:1], v[74:75], v[2:3], v[0:1]
	v_bitop3_b32 v37, v27, 24, 8 bitop3:0xc8
	v_pk_fma_f32 v[0:1], v[76:77], v[148:149], v[0:1]
	v_lshl_or_b32 v6, v5, 3, v93
	v_pk_fma_f32 v[0:1], v[78:79], v[150:151], v[0:1]
	v_or3_b32 v37, v85, v37, v87
	v_mul_f32_e32 v2, 0xbfb8aa3b, v0
	v_mul_f32_e32 v3, 0xbfb8aa3b, v1
	v_exp_f32_e32 v2, v2
	v_exp_f32_e32 v3, v3
	v_ashrrev_i32_e32 v7, 31, v6
	v_lshl_add_u64 v[124:125], v[6:7], 1, v[66:67]
	v_add_f32_e32 v2, 1.0, v2
	v_add_f32_e32 v3, 1.0, v3
	v_rcp_f32_e32 v2, v2
	v_rcp_f32_e32 v3, v3
	v_mul_f32_e32 v116, 0x3db504f3, v128
	v_mul_f32_e32 v122, 0x3db504f3, v129
	v_and_b32_e32 v200, 8, v175
	v_pk_mul_f32 v[126:127], v[0:1], v[2:3]
	v_bitop3_b32 v2, v27, 23, 7 bitop3:0xc8
	v_mul_f32_e32 v0, v127, v127
	v_pk_fma_f32 v[144:145], v[126:127], v[126:127], v[0:1] op_sel_hi:[1,1,0]
	v_pk_mul_f32 v[0:1], v[80:81], v[148:149]
	v_pk_fma_f32 v[148:149], v[74:75], v[148:149], v[154:155]
	v_pk_fma_f32 v[0:1], v[74:75], v[130:131], v[0:1]
	v_pk_fma_f32 v[148:149], v[76:77], v[152:153], v[148:149]
	v_pk_fma_f32 v[0:1], v[76:77], v[150:151], v[0:1]
	v_pk_fma_f32 v[148:149], v[78:79], v[202:203], v[148:149]
	v_pk_fma_f32 v[0:1], v[78:79], v[152:153], v[0:1]
	v_mul_f32_e32 v133, 0xbfb8aa3b, v148
	v_exp_f32_e32 v133, v133
	v_mul_f32_e32 v135, 0xbfb8aa3b, v149
	v_exp_f32_e32 v135, v135
	v_mul_f32_e32 v3, 0xbfb8aa3b, v0
	v_add_f32_e32 v133, 1.0, v133
	v_rcp_f32_e32 v204, v133
	v_add_f32_e32 v133, 1.0, v135
	v_rcp_f32_e32 v205, v133
	v_mul_f32_e32 v5, 0xbfb8aa3b, v1
	v_exp_f32_e32 v3, v3
	v_exp_f32_e32 v5, v5
	v_pk_mul_f32 v[148:149], v[148:149], v[204:205]
	v_lshl_or_b32 v154, v37, 3, v93
	v_mul_f32_e32 v204, v149, v149
	v_pk_fma_f32 v[204:205], v[148:149], v[148:149], v[204:205] op_sel_hi:[1,1,0]
	v_or3_b32 v6, v85, v2, v87
	s_nop 0
	v_permlane32_swap_b32_e32 v138, v204
	v_add_f32_e32 v37, v138, v204
	v_lshlrev_b32_e32 v204, 16, v156
	v_and_b32_e32 v205, 0xffff0000, v156
	v_pk_mul_f32 v[156:157], v[80:81], v[152:153]
	v_add_f32_e32 v2, 1.0, v3
	v_pk_fma_f32 v[150:151], v[74:75], v[150:151], v[156:157]
	v_add_f32_e32 v3, 1.0, v5
	v_pk_fma_f32 v[150:151], v[76:77], v[202:203], v[150:151]
	v_rcp_f32_e32 v2, v2
	v_pk_fma_f32 v[150:151], v[78:79], v[204:205], v[150:151]
	v_rcp_f32_e32 v3, v3
	v_mul_f32_e32 v133, 0xbfb8aa3b, v150
	v_exp_f32_e32 v133, v133
	v_mul_f32_e32 v135, 0xbfb8aa3b, v151
	v_exp_f32_e32 v135, v135
	v_lshl_or_b32 v6, v6, 3, v93
	v_pk_mul_f32 v[130:131], v[0:1], v[2:3]
	v_add_f32_e32 v133, 1.0, v133
	v_ashrrev_i32_e32 v7, 31, v6
	v_mul_f32_e32 v0, v131, v131
	v_rcp_f32_e32 v208, v133
	v_add_f32_e32 v133, 1.0, v135
	v_lshl_add_u64 v[128:129], v[6:7], 1, v[66:67]
	v_pk_fma_f32 v[6:7], v[130:131], v[130:131], v[0:1] op_sel_hi:[1,1,0]
	v_lshl_add_u32 v0, v192, 2, v29
	v_rcp_f32_e32 v209, v133
	ds_read_b128 v[0:3], v0 offset:512
	v_permlane32_swap_b32_e32 v4, v6
	v_pk_mul_f32 v[150:151], v[150:151], v[208:209]
	v_add_f32_e32 v9, v4, v6
	v_lshl_add_u32 v4, v51, 2, v29
	v_mul_f32_e32 v208, v151, v151
	ds_read_b128 v[4:7], v4 offset:512
	s_waitcnt lgkmcnt(1)
; DI float bflo(unsigned u) { return __uint_as_float(u << 16); }
; DI float bfhi(unsigned u) { return __uint_as_float(u & 0xffff0000u); }
; DI float dpp_xor8(float v) { return __uint_as_float((unsigned)__builtin_amdgcn_update_dpp(0, (int)__float_as_uint(v), 0x128, 0xF, 0xF, true)); }
; DI float swap32sum(float a, float b) { const auto r = __builtin_amdgcn_permlane32_swap(__float_as_uint(a), __float_as_uint(b), false, false); return __uint_as_float(r[0]) + __uint_as_float(r[1]); }
; DI float swap16sum(float a, float b) { const auto r = __builtin_amdgcn_permlane16_swap(__float_as_uint(a), __float_as_uint(b), false, false); return __uint_as_float(r[0]) + __uint_as_float(r[1]); }
; DI float sigmoidf_(float x) { return __builtin_amdgcn_rcpf(1.f + __expf(-x)); }
; DI void gdn_prep_unit(const Params& p, int U, char* lds) {
;     ...
;       for (int ii = 0; ii < 16; ++ii) {
;         float a0 = w0[0] * bflo(raw[ii]) + w0[1] * bflo(raw[ii + 1]) + w0[2] * bflo(raw[ii + 2]) + w0[3] * bflo(raw[ii + 3]);
;         float a1 = w1[0] * bfhi(raw[ii]) + w1[1] * bfhi(raw[ii + 1]) + w1[2] * bfhi(raw[ii + 2]) + w1[3] * bfhi(raw[ii + 3]);
;         a0 = a0 * sigmoidf_(a0); a1 = a1 * sigmoidf_(a1);
;         y0[ii] = a0; y1[ii] = a1; ssr[ii] = a0 * a0 + a1 * a1;
;       }
;       if (X < 2) {
;         const bool b3 = (lane & 8) != 0, b2 = (lane & 4) != 0;
;         float r8[8], r4[4], r2[2];
; #pragma unroll
;         for (int j = 0; j < 8; ++j) r8[j] = swap32sum(ssr[j], ssr[8 + j]);
; #pragma unroll
;         for (int j = 0; j < 4; ++j) r4[j] = swap16sum(r8[j], r8[4 + j]);
; #pragma unroll
;         for (int j = 0; j < 2; ++j) { const float keep = b3 ? r4[2 + j] : r4[j], send = b3 ? r4[j] : r4[2 + j]; r2[j] = keep + dpp_xor8(send); }
;         float r1 = (b2 ? r2[1] : r2[0]) + __shfl_xor(b2 ? r2[0] : r2[1], 4);
;         r1 += __uint_as_float((unsigned)__builtin_amdgcn_update_dpp(0, (int)__float_as_uint(r1), 0x4E, 0xF, 0xF, true));
;         r1 += __uint_as_float((unsigned)__builtin_amdgcn_update_dpp(0, (int)__float_as_uint(r1), 0xB1, 0xF, 0xF, true));
; #pragma unroll
;         for (int ii = 0; ii < 16; ++ii) ssr[ii] = __uint_as_float((unsigned)__builtin_amdgcn_readlane((int)__float_as_uint(r1), 4 * ii));
	v_mul_f32_e32 v138, 0x3db504f3, v1
	v_bitop3_b32 v1, v27, 25, 9 bitop3:0xc8
	v_pk_fma_f32 v[208:209], v[150:151], v[150:151], v[208:209] op_sel_hi:[1,1,0]
	v_or3_b32 v1, v85, v1, v87
	s_nop 0
	v_permlane32_swap_b32_e32 v136, v208
	v_lshl_or_b32 v156, v1, 3, v93
	v_add_f32_e32 v1, v136, v208
	v_pk_mul_f32 v[136:137], v[80:81], v[202:203]
	v_lshlrev_b32_e32 v208, 16, v159
	v_pk_fma_f32 v[136:137], v[74:75], v[152:153], v[136:137]
	v_and_b32_e32 v209, 0xffff0000, v159
	v_pk_fma_f32 v[136:137], v[76:77], v[204:205], v[136:137]
	v_bitop3_b32 v133, v27, 26, 10 bitop3:0xc8
	v_pk_fma_f32 v[136:137], v[78:79], v[208:209], v[136:137]
	v_or3_b32 v133, v85, v133, v87
	v_mul_f32_e32 v135, 0xbfb8aa3b, v136
	v_exp_f32_e32 v135, v135
	v_mul_f32_e32 v139, 0xbfb8aa3b, v137
	v_exp_f32_e32 v139, v139
	v_lshl_or_b32 v152, v133, 3, v93
	v_add_f32_e32 v135, 1.0, v135
	v_rcp_f32_e32 v210, v135
	v_add_f32_e32 v135, 1.0, v139
	v_rcp_f32_e32 v211, v135
	v_bitop3_b32 v133, v27, 27, 11 bitop3:0xc8
	v_or3_b32 v133, v85, v133, v87
	v_cmp_eq_u32_e64 s[0:1], 0, v200
	v_pk_mul_f32 v[136:137], v[136:137], v[210:211]
	v_cmp_eq_u32_e64 s[12:13], 0, v99
	v_mul_f32_e32 v210, v137, v137
	v_pk_fma_f32 v[210:211], v[136:137], v[136:137], v[210:211] op_sel_hi:[1,1,0]
	v_ashrrev_i32_e32 v91, 31, v90
	s_nop 0
	v_permlane32_swap_b32_e32 v134, v210
	v_add_f32_e32 v139, v134, v210
	v_pk_mul_f32 v[134:135], v[80:81], v[204:205]
	v_lshlrev_b32_e32 v210, 16, v158
	v_pk_fma_f32 v[134:135], v[74:75], v[202:203], v[134:135]
	v_and_b32_e32 v211, 0xffff0000, v158
	v_pk_fma_f32 v[134:135], v[76:77], v[208:209], v[134:135]
	v_lshl_or_b32 v158, v133, 3, v93
	v_pk_fma_f32 v[134:135], v[78:79], v[210:211], v[134:135]
	v_lshl_add_u64 v[90:91], v[90:91], 1, v[66:67]
	v_mul_f32_e32 v141, 0xbfb8aa3b, v134
	v_exp_f32_e32 v141, v141
	v_mul_f32_e32 v143, 0xbfb8aa3b, v135
	v_exp_f32_e32 v143, v143
	v_ashrrev_i32_e32 v97, 31, v96
	v_add_f32_e32 v141, 1.0, v141
	v_rcp_f32_e32 v202, v141
	v_add_f32_e32 v141, 1.0, v143
	v_rcp_f32_e32 v203, v141
	v_bitop3_b32 v141, v27, 28, 12 bitop3:0xc8
	v_or3_b32 v141, v85, v141, v87
	v_lshl_add_u64 v[96:97], v[96:97], 1, v[66:67]
	v_pk_mul_f32 v[134:135], v[134:135], v[202:203]
	v_ashrrev_i32_e32 v103, 31, v102
	v_mul_f32_e32 v202, v135, v135
	v_pk_fma_f32 v[202:203], v[134:135], v[134:135], v[202:203] op_sel_hi:[1,1,0]
	v_lshl_add_u64 v[102:103], v[102:103], 1, v[66:67]
	s_nop 0
	v_permlane32_swap_b32_e32 v132, v202
	v_add_f32_e32 v132, v132, v202
	s_nop 1
	v_permlane16_swap_b32_e32 v9, v132
	v_add_f32_e32 v9, v9, v132
	v_pk_mul_f32 v[132:133], v[80:81], v[208:209]
	v_lshlrev_b32_e32 v202, 16, v160
	v_pk_fma_f32 v[132:133], v[74:75], v[204:205], v[132:133]
	v_and_b32_e32 v203, 0xffff0000, v160
	v_pk_fma_f32 v[132:133], v[76:77], v[210:211], v[132:133]
	v_lshl_or_b32 v160, v141, 3, v93
	v_pk_fma_f32 v[132:133], v[78:79], v[202:203], v[132:133]
	v_ashrrev_i32_e32 v109, 31, v108
	v_mul_f32_e32 v143, 0xbfb8aa3b, v132
	v_exp_f32_e32 v143, v143
	v_mul_f32_e32 v145, 0xbfb8aa3b, v133
	v_exp_f32_e32 v145, v145
	v_lshl_add_u64 v[108:109], v[108:109], 1, v[66:67]
	v_add_f32_e32 v143, 1.0, v143
	v_rcp_f32_e32 v204, v143
	v_add_f32_e32 v143, 1.0, v145
	v_rcp_f32_e32 v205, v143
	v_bitop3_b32 v143, v27, 29, 13 bitop3:0xc8
	v_or3_b32 v143, v85, v143, v87
	v_ashrrev_i32_e32 v113, 31, v112
	v_pk_mul_f32 v[132:133], v[132:133], v[204:205]
	v_lshl_add_u64 v[112:113], v[112:113], 1, v[66:67]
	v_mul_f32_e32 v204, v133, v133
	v_pk_fma_f32 v[204:205], v[132:133], v[132:133], v[204:205] op_sel_hi:[1,1,0]
	v_ashrrev_i32_e32 v119, 31, v118
	s_nop 0
	v_permlane32_swap_b32_e32 v140, v204
	v_add_f32_e32 v140, v140, v204
	s_nop 1
	v_permlane16_swap_b32_e32 v37, v140
	v_add_f32_e32 v37, v37, v140
	v_pk_mul_f32 v[140:141], v[80:81], v[210:211]
	v_lshlrev_b32_e32 v204, 16, v162
	v_pk_fma_f32 v[140:141], v[74:75], v[208:209], v[140:141]
	v_and_b32_e32 v205, 0xffff0000, v162
	v_pk_fma_f32 v[140:141], v[76:77], v[202:203], v[140:141]
	v_pk_mul_f32 v[80:81], v[80:81], v[202:203]
	v_pk_fma_f32 v[140:141], v[78:79], v[204:205], v[140:141]
	v_pk_fma_f32 v[74:75], v[74:75], v[210:211], v[80:81]
	v_mul_f32_e32 v145, 0xbfb8aa3b, v140
	v_exp_f32_e32 v145, v145
	v_mul_f32_e32 v162, 0xbfb8aa3b, v141
	v_exp_f32_e32 v162, v162
	v_pk_fma_f32 v[74:75], v[76:77], v[204:205], v[74:75]
	v_add_f32_e32 v145, 1.0, v145
	v_rcp_f32_e32 v208, v145
	v_add_f32_e32 v145, 1.0, v162
	v_rcp_f32_e32 v209, v145
	v_lshl_or_b32 v162, v143, 3, v93
	v_and_b32_e32 v143, 0xffff0000, v71
	v_lshl_add_u64 v[118:119], v[118:119], 1, v[66:67]
	v_pk_mul_f32 v[140:141], v[140:141], v[208:209]
	v_mul_f32_e32 v0, 0x3db504f3, v0
	v_mul_f32_e32 v208, v141, v141
	v_pk_fma_f32 v[208:209], v[140:141], v[140:141], v[208:209] op_sel_hi:[1,1,0]
	v_ashrrev_i32_e32 v155, 31, v154
	s_nop 0
	v_permlane32_swap_b32_e32 v142, v208
	v_add_f32_e32 v142, v142, v208
	s_nop 1
	v_permlane16_swap_b32_e32 v1, v142
	v_add_f32_e32 v1, v1, v142
	v_lshlrev_b32_e32 v142, 16, v71
	v_pk_fma_f32 v[74:75], v[78:79], v[142:143], v[74:75]
	v_cndmask_b32_e64 v78, v1, v9, s[0:1]
	v_mul_f32_e32 v71, 0xbfb8aa3b, v74
	v_exp_f32_e32 v71, v71
	v_mul_f32_e32 v76, 0xbfb8aa3b, v75
	v_exp_f32_e32 v77, v76
	v_cndmask_b32_e64 v1, v9, v1, s[0:1]
	v_add_f32_e32 v71, 1.0, v71
	v_rcp_f32_e32 v76, v71
	v_add_f32_e32 v71, 1.0, v77
	v_rcp_f32_e32 v77, v71
	v_add_f32_dpp v1, v1, v78 row_ror:8 row_mask:0xf bank_mask:0xf bound_ctrl:1
	v_bitop3_b32 v9, v27, 30, 14 bitop3:0xc8
	v_or3_b32 v9, v85, v9, v87
	v_pk_mul_f32 v[74:75], v[74:75], v[76:77]
	v_lshl_add_u64 v[154:155], v[154:155], 1, v[66:67]
	v_mul_f32_e32 v76, v75, v75
	v_pk_fma_f32 v[76:77], v[74:75], v[74:75], v[76:77] op_sel_hi:[1,1,0]
	v_ashrrev_i32_e32 v157, 31, v156
	s_nop 0
	v_permlane32_swap_b32_e32 v144, v76
	v_add_f32_e32 v71, v144, v76
	s_nop 1
	v_permlane16_swap_b32_e32 v139, v71
	v_add_f32_e32 v71, v139, v71
	v_cndmask_b32_e64 v76, v71, v37, s[0:1]
	v_cndmask_b32_e64 v37, v37, v71, s[0:1]
	v_lshl_add_u64 v[156:157], v[156:157], 1, v[66:67]
	v_mul_f32_e32 v2, 0x3db504f3, v2
	v_add_f32_dpp v37, v37, v76 row_ror:8 row_mask:0xf bank_mask:0xf bound_ctrl:1
	v_cndmask_b32_e64 v71, v37, v1, s[12:13]
	v_cndmask_b32_e64 v1, v1, v37, s[12:13]
	ds_bpermute_b32 v1, v55, v1
	v_lshl_or_b32 v76, v9, 3, v93
	v_ashrrev_i32_e32 v153, 31, v152
	v_lshl_add_u64 v[152:153], v[152:153], 1, v[66:67]
	v_ashrrev_i32_e32 v159, 31, v158
	s_waitcnt lgkmcnt(0)
; DI unsigned pk2(float lo, float hi) { f32x2 v = {lo, hi}; bf16x2_t b = __builtin_convertvector(v, bf16x2_t); return __builtin_bit_cast(unsigned, b); }
; DI void gdn_prep_unit(const Params& p, int U, char* lds) {
;     ...
;         float r1 = (b2 ? r2[1] : r2[0]) + __shfl_xor(b2 ? r2[0] : r2[1], 4);
;         r1 += __uint_as_float((unsigned)__builtin_amdgcn_update_dpp(0, (int)__float_as_uint(r1), 0x4E, 0xF, 0xF, true));
;         r1 += __uint_as_float((unsigned)__builtin_amdgcn_update_dpp(0, (int)__float_as_uint(r1), 0xB1, 0xF, 0xF, true));
; #pragma unroll
;         for (int ii = 0; ii < 16; ++ii) ssr[ii] = __uint_as_float((unsigned)__builtin_amdgcn_readlane((int)__float_as_uint(r1), 4 * ii));
;       }
; #pragma unroll
;       for (int ii = 0; ii < 16; ++ii) {
;         const int i = i0 + ii;
;         float a0 = y0[ii], a1 = y1[ii];
;         if (X < 2) { const float rn = rsqrtf(ssr[ii] + 1e-6f); a0 *= rn; a1 *= rn; }
;         *(unsigned*)(dst + i * QP + 2 * lane) = pk2(a0, a1);
;         if (X == 0) {
;           const float f = 0.08838834764831845f * gcs[128 + i];
;           const int d = 2 * lane, mm = d >> 5, ss2 = (d >> 4) & 1, aa = (d >> 3) & 1, hh = (d >> 2) & 1, bb = d & 3;
;           const int lp = (i & 31) + 32 * hh;
;           *(unsigned*)(QF + (size_t)(((((i >> 5) * 4 + mm) * 2 + ss2) * 64 + lp) * 8 + 4 * aa + bb)) = pk2(a0 * f, a1 * f);
;         }
	v_add_f32_e32 v1, v71, v1
	v_lshl_add_u64 v[158:159], v[158:159], 1, v[66:67]
	v_ashrrev_i32_e32 v161, 31, v160
	v_add_f32_dpp v1, v1, v1 quad_perm:[2,3,0,1] row_mask:0xf bank_mask:0xf bound_ctrl:1
	v_lshl_add_u64 v[160:161], v[160:161], 1, v[66:67]
	v_ashrrev_i32_e32 v163, 31, v162
	v_add_f32_dpp v1, v1, v1 quad_perm:[1,0,3,2] row_mask:0xf bank_mask:0xf bound_ctrl:1
	v_lshl_add_u64 v[162:163], v[162:163], 1, v[66:67]
	v_readlane_b32 s15, v1, 0
	v_readlane_b32 s14, v1, 4
	v_readlane_b32 s75, v1, 8
	v_readlane_b32 s74, v1, 12
	v_pk_add_f32 v[78:79], s[14:15], v[32:33] op_sel_hi:[1,0]
	v_readlane_b32 s79, v1, 16
	v_mul_f32_e32 v9, 0x4b800000, v79
	v_cmp_gt_f32_e64 s[14:15], s19, v79
	v_readlane_b32 s78, v1, 20
	v_readlane_b32 s81, v1, 24
	v_cndmask_b32_e64 v9, v79, v9, s[14:15]
	v_rsq_f32_e32 v9, v9
	v_readlane_b32 s80, v1, 28
	v_readlane_b32 s61, v1, 32
	v_readlane_b32 s60, v1, 36
	v_readlane_b32 s51, v1, 40
	v_readlane_b32 s50, v1, 44
	v_readlane_b32 s49, v1, 48
	v_readlane_b32 s48, v1, 52
	v_readlane_b32 s45, v1, 56
	v_readlane_b32 s44, v1, 60
	v_mul_f32_e32 v1, 0x45800000, v9
	v_cndmask_b32_e64 v80, v9, v1, s[14:15]
	v_pk_mul_f32 v[80:81], v[80:81], v[82:83] op_sel_hi:[0,1]
	v_cvt_pk_bf16_f32 v1, v80, v81
	ds_write_b32 v8, v1
	v_mul_f32_e32 v1, 0x4b800000, v78
	v_cmp_gt_f32_e64 s[14:15], s19, v78
	v_ashrrev_i32_e32 v77, 31, v76
	v_lshl_add_u64 v[76:77], v[76:77], 1, v[66:67]
	v_cndmask_b32_e64 v1, v78, v1, s[14:15]
	v_rsq_f32_e32 v1, v1
	v_pk_mul_f32 v[78:79], v[80:81], v[84:85] op_sel_hi:[1,0]
	v_pk_add_f32 v[80:81], s[74:75], v[32:33] op_sel_hi:[1,0]
	v_cvt_pk_bf16_f32 v9, v78, v79
	global_store_dword v[90:91], v9, off
	v_mul_f32_e32 v9, 0x45800000, v1
	v_cndmask_b32_e64 v78, v1, v9, s[14:15]
	v_mul_f32_e32 v9, 0x4b800000, v81
	v_cmp_gt_f32_e64 s[14:15], s19, v81
	v_pk_mul_f32 v[78:79], v[78:79], v[88:89] op_sel_hi:[0,1]
	v_cvt_pk_bf16_f32 v1, v78, v79
	v_cndmask_b32_e64 v9, v81, v9, s[14:15]
	v_rsq_f32_e32 v9, v9
	v_pk_mul_f32 v[78:79], v[78:79], v[86:87] op_sel_hi:[1,0]
	s_nop 0
	v_cvt_pk_bf16_f32 v37, v78, v79
	global_store_dword v[96:97], v37, off
	v_mul_f32_e32 v37, 0x45800000, v9
	v_cndmask_b32_e64 v78, v9, v37, s[14:15]
	v_pk_mul_f32 v[78:79], v[78:79], v[94:95] op_sel_hi:[0,1]
	v_cvt_pk_bf16_f32 v9, v78, v79
	ds_write2_b32 v36, v1, v9 offset1:68
	v_mul_f32_e32 v1, 0x4b800000, v80
	v_cmp_gt_f32_e64 s[14:15], s19, v80
	v_pk_mul_f32 v[78:79], v[78:79], v[92:93] op_sel_hi:[1,0]
	s_nop 0
	v_cndmask_b32_e64 v1, v80, v1, s[14:15]
	v_rsq_f32_e32 v1, v1
	v_cvt_pk_bf16_f32 v9, v78, v79
	global_store_dword v[102:103], v9, off
	v_pk_add_f32 v[80:81], s[78:79], v[32:33] op_sel_hi:[1,0]
	v_mul_f32_e32 v9, 0x45800000, v1
	v_cndmask_b32_e64 v78, v1, v9, s[14:15]
	v_mul_f32_e32 v9, 0x4b800000, v81
	v_cmp_gt_f32_e64 s[14:15], s19, v81
	v_pk_mul_f32 v[78:79], v[78:79], v[100:101] op_sel_hi:[0,1]
	v_cvt_pk_bf16_f32 v1, v78, v79
	v_cndmask_b32_e64 v9, v81, v9, s[14:15]
	v_rsq_f32_e32 v9, v9
	v_pk_mul_f32 v[78:79], v[78:79], v[98:99] op_sel_hi:[1,0]
	s_nop 0
	v_cvt_pk_bf16_f32 v37, v78, v79
	global_store_dword v[108:109], v37, off
	v_mul_f32_e32 v37, 0x45800000, v9
	v_cndmask_b32_e64 v78, v9, v37, s[14:15]
	v_pk_mul_f32 v[78:79], v[78:79], v[106:107] op_sel_hi:[0,1]
	v_cvt_pk_bf16_f32 v9, v78, v79
	ds_write2_b32 v36, v1, v9 offset0:136 offset1:204
	v_mul_f32_e32 v1, 0x4b800000, v80
	v_cmp_gt_f32_e64 s[14:15], s19, v80
	v_pk_mul_f32 v[78:79], v[78:79], v[104:105] op_sel_hi:[1,0]
	s_nop 0
	v_cndmask_b32_e64 v1, v80, v1, s[14:15]
	v_rsq_f32_e32 v1, v1
	v_cvt_pk_bf16_f32 v9, v78, v79
	global_store_dword v[112:113], v9, off
	v_pk_add_f32 v[80:81], s[80:81], v[32:33] op_sel_hi:[1,0]
	v_mul_f32_e32 v9, 0x45800000, v1
	v_cndmask_b32_e64 v78, v1, v9, s[14:15]
	v_mul_f32_e32 v9, 0x4b800000, v81
	v_cmp_gt_f32_e64 s[14:15], s19, v81
	v_pk_mul_f32 v[78:79], v[78:79], v[114:115] op_sel_hi:[0,1]
	v_cvt_pk_bf16_f32 v1, v78, v79
	v_cndmask_b32_e64 v9, v81, v9, s[14:15]
	v_rsq_f32_e32 v9, v9
	v_pk_mul_f32 v[78:79], v[78:79], v[110:111] op_sel_hi:[1,0]
	s_nop 0
	v_cvt_pk_bf16_f32 v37, v78, v79
	global_store_dword v[118:119], v37, off
	v_mul_f32_e32 v37, 0x45800000, v9
	v_cndmask_b32_e64 v78, v9, v37, s[14:15]
	v_pk_mul_f32 v[78:79], v[78:79], v[120:121] op_sel_hi:[0,1]
	v_cvt_pk_bf16_f32 v9, v78, v79
	v_add_u32_e32 v37, 0x400, v36
	ds_write2_b32 v37, v1, v9 offset0:16 offset1:84
	v_mul_f32_e32 v1, 0x4b800000, v80
	v_cmp_gt_f32_e64 s[14:15], s19, v80
	v_pk_mul_f32 v[78:79], v[78:79], v[116:117] op_sel_hi:[1,0]
	s_nop 0
	v_cndmask_b32_e64 v1, v80, v1, s[14:15]
	v_rsq_f32_e32 v1, v1
	v_cvt_pk_bf16_f32 v9, v78, v79
	global_store_dword v[124:125], v9, off
	v_pk_add_f32 v[80:81], s[60:61], v[32:33] op_sel_hi:[1,0]
	v_mul_f32_e32 v9, 0x45800000, v1
	v_cndmask_b32_e64 v78, v1, v9, s[14:15]
	v_mul_f32_e32 v9, 0x4b800000, v81
	v_cmp_gt_f32_e64 s[14:15], s19, v81
	v_pk_mul_f32 v[78:79], v[78:79], v[126:127] op_sel_hi:[0,1]
	v_cvt_pk_bf16_f32 v1, v78, v79
	v_cndmask_b32_e64 v9, v81, v9, s[14:15]
	v_rsq_f32_e32 v9, v9
	v_pk_mul_f32 v[78:79], v[78:79], v[122:123] op_sel_hi:[1,0]
	s_nop 0
	v_cvt_pk_bf16_f32 v71, v78, v79
	global_store_dword v[128:129], v71, off
	v_mul_f32_e32 v71, 0x45800000, v9
	v_cndmask_b32_e64 v78, v9, v71, s[14:15]
	v_pk_mul_f32 v[78:79], v[78:79], v[130:131] op_sel_hi:[0,1]
	v_cvt_pk_bf16_f32 v9, v78, v79
	ds_write2_b32 v37, v1, v9 offset0:152 offset1:220
	v_mul_f32_e32 v1, 0x4b800000, v80
	v_cmp_gt_f32_e64 s[14:15], s19, v80
	v_add_u32_e32 v71, 0x800, v36
	s_nop 0
	v_cndmask_b32_e64 v1, v80, v1, s[14:15]
	v_rsq_f32_e32 v9, v1
	v_pk_mul_f32 v[0:1], v[78:79], v[0:1] op_sel_hi:[1,0]
	v_pk_add_f32 v[78:79], s[50:51], v[32:33] op_sel_hi:[1,0]
; DI void gdn_prep_unit(const Params& p, int U, char* lds) {
;     ...
;     for (int X = 0; X < 3; ++X) {
;       const int col = 1536 + 512 * X + h * 128 + 2 * lane, cb = 512 * X + h * 128 + 2 * lane;
;       float w0[4], w1[4];
; #pragma unroll
;       for (int j = 0; j < 4; ++j) { w0[j] = p.conv_w[j * 1536 + cb]; w1[j] = p.conv_w[j * 1536 + cb + 1]; }
;       bf16_t* dst = X == 0 ? q_s : (X == 1 ? k_s : v_s);
;       const int i0 = 16 * wid;
;       unsigned raw[19];
;       {
;         const unsigned* pr[19];
; #pragma unroll
;         for (int j = 0; j < 19; ++j) { const int rr = i0 - 3 + j; const int rc = (s0 + rr >= 0) ? rr : -s0;
;           pr[j] = (const unsigned*)(proj + (size_t)((long)t0 + rc) * PP + col); }
;         asm volatile("global_load_dword %0, %10, off\n\tglobal_load_dword %1, %11, off\n\tglobal_load_dword %2, %12, off\n\tglobal_load_dword %3, %13, off\n\tglobal_load_dword %4, %14, off\n\t"
;                      "global_load_dword %5, %15, off\n\tglobal_load_dword %6, %16, off\n\tglobal_load_dword %7, %17, off\n\tglobal_load_dword %8, %18, off\n\tglobal_load_dword %9, %19, off\n\ts_waitcnt vmcnt(0)"
;                      : "=&v"(raw[0]), "=&v"(raw[1]), "=&v"(raw[2]), "=&v"(raw[3]), "=&v"(raw[4]), "=&v"(raw[5]), "=&v"(raw[6]), "=&v"(raw[7]), "=&v"(raw[8]), "=&v"(raw[9])
;                      : "v"(pr[0]), "v"(pr[1]), "v"(pr[2]), "v"(pr[3]), "v"(pr[4]), "v"(pr[5]), "v"(pr[6]), "v"(pr[7]), "v"(pr[8]), "v"(pr[9]) : "memory");
;         asm volatile("global_load_dword %0, %9, off\n\tglobal_load_dword %1, %10, off\n\tglobal_load_dword %2, %11, off\n\tglobal_load_dword %3, %12, off\n\tglobal_load_dword %4, %13, off\n\t"
;     ...
;       for (int ii = 0; ii < 16; ++ii) {
;         const int i = i0 + ii;
;         float a0 = y0[ii], a1 = y1[ii];
;         if (X < 2) { const float rn = rsqrtf(ssr[ii] + 1e-6f); a0 *= rn; a1 *= rn; }
;         *(unsigned*)(dst + i * QP + 2 * lane) = pk2(a0, a1);
;         if (X == 0) {
;           const float f = 0.08838834764831845f * gcs[128 + i];
;           const int d = 2 * lane, mm = d >> 5, ss2 = (d >> 4) & 1, aa = (d >> 3) & 1, hh = (d >> 2) & 1, bb = d & 3;
;           const int lp = (i & 31) + 32 * hh;
;           *(unsigned*)(QF + (size_t)(((((i >> 5) * 4 + mm) * 2 + ss2) * 64 + lp) * 8 + 4 * aa + bb)) = pk2(a0 * f, a1 * f);
;         }
	v_cvt_pk_bf16_f32 v0, v0, v1
	global_store_dword v[154:155], v0, off
	v_mul_f32_e32 v0, 0x45800000, v9
	v_cndmask_b32_e64 v0, v9, v0, s[14:15]
	v_mul_f32_e32 v37, 0x4b800000, v79
	v_cmp_gt_f32_e64 s[14:15], s19, v79
	v_pk_mul_f32 v[0:1], v[0:1], v[148:149] op_sel_hi:[0,1]
	v_cvt_pk_bf16_f32 v9, v0, v1
	v_cndmask_b32_e64 v37, v79, v37, s[14:15]
	v_rsq_f32_e32 v37, v37
	v_pk_mul_f32 v[0:1], v[0:1], v[138:139] op_sel_hi:[1,0]
	s_nop 0
	v_cvt_pk_bf16_f32 v0, v0, v1
	global_store_dword v[156:157], v0, off
	v_mul_f32_e32 v0, 0x45800000, v37
	v_cndmask_b32_e64 v0, v37, v0, s[14:15]
	v_pk_mul_f32 v[0:1], v[150:151], v[0:1] op_sel_hi:[1,0]
	v_cmp_gt_f32_e64 s[14:15], s19, v78
	v_cvt_pk_bf16_f32 v37, v0, v1
	ds_write2_b32 v71, v9, v37 offset0:32 offset1:100
	v_mul_f32_e32 v9, 0x4b800000, v78
	v_cndmask_b32_e64 v9, v78, v9, s[14:15]
	v_rsq_f32_e32 v9, v9
	v_pk_mul_f32 v[0:1], v[0:1], v[2:3] op_sel_hi:[1,0]
	v_mul_f32_e32 v2, 0x3db504f3, v3
	v_cvt_pk_bf16_f32 v0, v0, v1
	global_store_dword v[152:153], v0, off
	v_mul_f32_e32 v0, 0x45800000, v9
	v_cndmask_b32_e64 v0, v9, v0, s[14:15]
	v_pk_mul_f32 v[0:1], v[136:137], v[0:1] op_sel_hi:[1,0]
	s_nop 0
	v_cvt_pk_bf16_f32 v9, v0, v1
	v_pk_mul_f32 v[0:1], v[0:1], v[2:3] op_sel_hi:[1,0]
	v_pk_add_f32 v[2:3], s[48:49], v[32:33] op_sel_hi:[1,0]
	v_cvt_pk_bf16_f32 v0, v0, v1
	v_mul_f32_e32 v37, 0x4b800000, v3
	v_cmp_gt_f32_e64 s[14:15], s19, v3
	global_store_dword v[158:159], v0, off
	v_mul_f32_e32 v0, 0x3db504f3, v4
	v_cndmask_b32_e64 v3, v3, v37, s[14:15]
	v_rsq_f32_e32 v3, v3
	s_nop 0
	v_mul_f32_e32 v1, 0x45800000, v3
	v_cndmask_b32_e64 v4, v3, v1, s[14:15]
	v_pk_mul_f32 v[78:79], v[134:135], v[4:5] op_sel_hi:[1,0]
	v_cmp_gt_f32_e64 s[14:15], s19, v2
	v_cvt_pk_bf16_f32 v1, v78, v79
	ds_write2_b32 v71, v9, v1 offset0:168 offset1:236
	v_mul_f32_e32 v1, 0x4b800000, v2
	v_cndmask_b32_e64 v1, v2, v1, s[14:15]
	v_rsq_f32_e32 v2, v1
	v_pk_mul_f32 v[0:1], v[78:79], v[0:1] op_sel_hi:[1,0]
	s_nop 0
	v_cvt_pk_bf16_f32 v0, v0, v1
	global_store_dword v[160:161], v0, off
	v_mul_f32_e32 v0, 0x45800000, v2
	v_cndmask_b32_e64 v0, v2, v0, s[14:15]
	v_pk_mul_f32 v[0:1], v[132:133], v[0:1] op_sel_hi:[1,0]
	v_mul_f32_e32 v2, 0x3db504f3, v5
	v_cvt_pk_bf16_f32 v9, v0, v1
	v_pk_mul_f32 v[0:1], v[0:1], v[2:3] op_sel_hi:[1,0]
	v_pk_add_f32 v[2:3], s[44:45], v[32:33] op_sel_hi:[1,0]
	v_cvt_pk_bf16_f32 v0, v0, v1
	v_mul_f32_e32 v4, 0x4b800000, v3
	v_cmp_gt_f32_e64 s[14:15], s19, v3
	global_store_dword v[162:163], v0, off
	v_mul_f32_e32 v0, 0x3db504f3, v6
	v_cndmask_b32_e64 v3, v3, v4, s[14:15]
	v_rsq_f32_e32 v3, v3
	s_nop 0
	v_mul_f32_e32 v1, 0x45800000, v3
	v_cndmask_b32_e64 v4, v3, v1, s[14:15]
	v_pk_mul_f32 v[4:5], v[140:141], v[4:5] op_sel_hi:[1,0]
	v_add_u32_e32 v3, 0xc00, v36
	v_cvt_pk_bf16_f32 v1, v4, v5
	ds_write2_b32 v3, v9, v1 offset0:48 offset1:116
	v_mul_f32_e32 v1, 0x4b800000, v2
	v_cmp_gt_f32_e64 s[14:15], s19, v2
	v_bitop3_b32 v9, v27, 31, 15 bitop3:0xc8
	v_or3_b32 v9, v85, v9, v87
	v_cndmask_b32_e64 v1, v2, v1, s[14:15]
	v_rsq_f32_e32 v2, v1
	v_pk_mul_f32 v[0:1], v[4:5], v[0:1] op_sel_hi:[1,0]
	s_nop 0
	v_cvt_pk_bf16_f32 v0, v0, v1
	global_store_dword v[76:77], v0, off
	v_mul_f32_e32 v0, 0x45800000, v2
	v_cndmask_b32_e64 v0, v2, v0, s[14:15]
	s_movk_i32 s14, 0x2000
	v_add_co_u32_e64 v2, s[14:15], s14, v68
	v_pk_mul_f32 v[74:75], v[74:75], v[0:1] op_sel_hi:[1,0]
	s_nop 0
	v_addc_co_u32_e64 v3, s[14:15], 0, v69, s[14:15]
	v_cvt_pk_bf16_f32 v0, v74, v75
	s_movk_i32 s14, 0x5000
	ds_write_b32 v36, v0 offset:3808
	v_add_co_u32_e64 v0, s[14:15], s14, v68
	v_mul_f32_e32 v76, 0x3db504f3, v7
	global_load_dwordx2 v[6:7], v[2:3], off
	global_load_dwordx2 v[4:5], v70, s[70:71] offset:2048
	s_nop 0
	global_load_dwordx2 v[70:71], v[72:73], off offset:2048
	v_addc_co_u32_e64 v1, s[14:15], 0, v69, s[14:15]
	global_load_dwordx2 v[68:69], v[0:1], off
	v_pk_mul_f32 v[72:73], v[74:75], v[76:77] op_sel_hi:[1,0]
	s_mov_b64 s[14:15], 0x1000
	v_cvt_pk_bf16_f32 v37, v72, v73
	v_lshl_or_b32 v72, v9, 3, v93
	v_ashrrev_i32_e32 v73, 31, v72
	v_lshl_add_u64 v[66:67], v[72:73], 1, v[66:67]
	global_store_dword v[66:67], v37, off
	v_lshl_add_u64 v[66:67], v[10:11], 0, s[14:15]
	v_mad_u64_u32 v[72:73], s[14:15], v12, s3, v[66:67]
	v_mad_u64_u32 v[74:75], s[14:15], v14, s3, v[66:67]
	v_mad_u64_u32 v[76:77], s[14:15], v16, s3, v[66:67]
	v_mad_u64_u32 v[78:79], s[14:15], v18, s3, v[66:67]
	v_mad_u64_u32 v[80:81], s[14:15], v20, s3, v[66:67]
	v_mad_u64_u32 v[82:83], s[14:15], v22, s3, v[66:67]
	v_mad_u64_u32 v[84:85], s[14:15], v24, s3, v[66:67]
	v_mad_u64_u32 v[86:87], s[14:15], v38, s3, v[66:67]
	v_mad_u64_u32 v[88:89], s[14:15], v40, s3, v[66:67]
	v_mad_u64_u32 v[90:91], s[14:15], v42, s3, v[66:67]
	v_add_u32_e32 v73, v13, v73
	v_add_u32_e32 v75, v15, v75
	v_add_u32_e32 v77, v17, v77
	v_add_u32_e32 v79, v19, v79
	v_add_u32_e32 v81, v21, v81
	v_add_u32_e32 v83, v23, v83
	v_add_u32_e32 v85, v25, v85
	v_add_u32_e32 v87, v39, v87
	v_add_u32_e32 v89, v193, v89
	v_add_u32_e32 v91, v194, v91
	v_mov_b32_e32 v9, v212
	v_mov_b32_e32 v37, v213
	v_mov_b32_e32 v104, v214
	v_mov_b32_e32 v110, v215
	v_mov_b32_e32 v112, v216
	v_mov_b32_e32 v113, v217
	v_mov_b32_e32 v114, v218
	v_mov_b32_e32 v115, v219
	v_mov_b32_e32 v116, v220
	v_mov_b32_e32 v118, v221
	s_waitcnt vmcnt(0)
; DI float bflo(unsigned u) { return __uint_as_float(u << 16); }
; DI void gdn_prep_unit(const Params& p, int U, char* lds) {
;     ...
;       for (int j = 0; j < 4; ++j) { w0[j] = p.conv_w[j * 1536 + cb]; w1[j] = p.conv_w[j * 1536 + cb + 1]; }
;       bf16_t* dst = X == 0 ? q_s : (X == 1 ? k_s : v_s);
;       const int i0 = 16 * wid;
;       unsigned raw[19];
;       {
;         const unsigned* pr[19];
; #pragma unroll
;         for (int j = 0; j < 19; ++j) { const int rr = i0 - 3 + j; const int rc = (s0 + rr >= 0) ? rr : -s0;
;           pr[j] = (const unsigned*)(proj + (size_t)((long)t0 + rc) * PP + col); }
;         asm volatile("global_load_dword %0, %10, off\n\tglobal_load_dword %1, %11, off\n\tglobal_load_dword %2, %12, off\n\tglobal_load_dword %3, %13, off\n\tglobal_load_dword %4, %14, off\n\t"
;                      "global_load_dword %5, %15, off\n\tglobal_load_dword %6, %16, off\n\tglobal_load_dword %7, %17, off\n\tglobal_load_dword %8, %18, off\n\tglobal_load_dword %9, %19, off\n\ts_waitcnt vmcnt(0)"
;                      : "=&v"(raw[0]), "=&v"(raw[1]), "=&v"(raw[2]), "=&v"(raw[3]), "=&v"(raw[4]), "=&v"(raw[5]), "=&v"(raw[6]), "=&v"(raw[7]), "=&v"(raw[8]), "=&v"(raw[9])
;                      : "v"(pr[0]), "v"(pr[1]), "v"(pr[2]), "v"(pr[3]), "v"(pr[4]), "v"(pr[5]), "v"(pr[6]), "v"(pr[7]), "v"(pr[8]), "v"(pr[9]) : "memory");
;         asm volatile("global_load_dword %0, %9, off\n\tglobal_load_dword %1, %10, off\n\tglobal_load_dword %2, %11, off\n\tglobal_load_dword %3, %12, off\n\tglobal_load_dword %4, %13, off\n\t"
;                      "global_load_dword %5, %14, off\n\tglobal_load_dword %6, %15, off\n\tglobal_load_dword %7, %16, off\n\tglobal_load_dword %8, %17, off\n\ts_waitcnt vmcnt(0)"
;                      : "=&v"(raw[10]), "=&v"(raw[11]), "=&v"(raw[12]), "=&v"(raw[13]), "=&v"(raw[14]), "=&v"(raw[15]), "=&v"(raw[16]), "=&v"(raw[17]), "=&v"(raw[18])
;                      : "v"(pr[10]), "v"(pr[11]), "v"(pr[12]), "v"(pr[13]), "v"(pr[14]), "v"(pr[15]), "v"(pr[16]), "v"(pr[17]), "v"(pr[18]) : "memory");
; #pragma unroll
;         for (int j = 0; j < 3; ++j) if (s0 + i0 - 3 + j < 0) raw[j] = 0u;
;       }
;       float y0[16], y1[16], ssr[16];
; #pragma unroll
;       for (int ii = 0; ii < 16; ++ii) {
;         float a0 = w0[0] * bflo(raw[ii]) + w0[1] * bflo(raw[ii + 1]) + w0[2] * bflo(raw[ii + 2]) + w0[3] * bflo(raw[ii + 3]);
	v_mad_u64_u32 v[92:93], s[14:15], v44, s3, v[66:67]
	v_cndmask_b32_e64 v37, v37, 0, s[8:9]
	v_cndmask_b32_e64 v9, v9, 0, vcc
	v_lshlrev_b32_e32 v74, 16, v37
	v_and_b32_e32 v75, 0xffff0000, v37
	v_cndmask_b32_e64 v78, v104, 0, s[10:11]
	v_lshlrev_b32_e32 v72, 16, v9
	v_and_b32_e32 v73, 0xffff0000, v9
	v_and_b32_e32 v79, 0xffff0000, v110
	v_mad_u64_u32 v[94:95], s[14:15], v46, s3, v[66:67]
	v_mad_u64_u32 v[96:97], s[14:15], v48, s3, v[66:67]
	v_mad_u64_u32 v[98:99], s[14:15], v50, s3, v[66:67]
	v_mad_u64_u32 v[100:101], s[14:15], v52, s3, v[66:67]
	v_mad_u64_u32 v[102:103], s[14:15], v54, s3, v[66:67]
	v_mad_u64_u32 v[106:107], s[14:15], v58, s3, v[66:67]
	v_mad_u64_u32 v[108:109], s[14:15], v60, s3, v[66:67]
	v_mad_u64_u32 v[66:67], s[14:15], v62, s3, v[66:67]
	v_add_u32_e32 v67, v63, v67
	v_add_u32_e32 v93, v45, v93
	v_add_u32_e32 v95, v195, v95
	v_add_u32_e32 v97, v196, v97
	v_add_u32_e32 v99, v197, v99
	v_add_u32_e32 v101, v198, v101
	v_add_u32_e32 v103, v199, v103
	v_add_u32_e32 v107, v59, v107
	v_add_u32_e32 v109, v61, v109
	s_waitcnt vmcnt(4)
	v_pk_mul_f32 v[76:77], v[6:7], v[74:75]
	s_waitcnt vmcnt(3)
	v_pk_fma_f32 v[72:73], v[4:5], v[72:73], v[76:77]
	v_lshlrev_b32_e32 v76, 16, v78
	v_and_b32_e32 v77, 0xffff0000, v78
	s_waitcnt vmcnt(2)
	v_pk_fma_f32 v[72:73], v[70:71], v[76:77], v[72:73]
	v_lshlrev_b32_e32 v78, 16, v110
	s_waitcnt vmcnt(1)
	v_pk_fma_f32 v[72:73], v[68:69], v[78:79], v[72:73]
	s_nop 0
	v_mul_f32_e32 v9, 0xbfb8aa3b, v72
	v_exp_f32_e32 v9, v9
	v_mul_f32_e32 v37, 0xbfb8aa3b, v73
	v_exp_f32_e32 v37, v37
	v_add_f32_e32 v9, 1.0, v9
	v_rcp_f32_e32 v80, v9
	v_add_f32_e32 v9, 1.0, v37
	v_rcp_f32_e32 v81, v9
	v_mov_b32_e32 v9, v222
	v_mov_b32_e32 v37, v223
	v_mov_b32_e32 v104, v224
	v_mov_b32_e32 v110, v225
	v_mov_b32_e32 v122, v226
	v_mov_b32_e32 v124, v227
	v_mov_b32_e32 v125, v228
	v_mov_b32_e32 v126, v229
	v_mov_b32_e32 v127, v230
	s_waitcnt vmcnt(0)
	v_lshlrev_b32_e32 v100, 16, v118
	v_and_b32_e32 v101, 0xffff0000, v118
	v_pk_mul_f32 v[66:67], v[72:73], v[80:81]
	v_pk_mul_f32 v[80:81], v[6:7], v[76:77]
	v_mul_f32_e32 v72, v67, v67
	v_pk_fma_f32 v[74:75], v[4:5], v[74:75], v[80:81]
	v_lshlrev_b32_e32 v80, 16, v112
	v_pk_fma_f32 v[74:75], v[70:71], v[78:79], v[74:75]
	v_and_b32_e32 v81, 0xffff0000, v112
	v_pk_fma_f32 v[74:75], v[68:69], v[80:81], v[74:75]
	v_pk_mul_f32 v[86:87], v[6:7], v[80:81]
	v_mul_f32_e32 v73, 0xbfb8aa3b, v74
	v_mul_f32_e32 v82, 0xbfb8aa3b, v75
	v_exp_f32_e32 v73, v73
	v_exp_f32_e32 v82, v82
	v_lshlrev_b32_e32 v112, 16, v37
	v_pk_fma_f32 v[88:89], v[66:67], v[66:67], v[72:73] op_sel_hi:[1,1,0]
	v_add_f32_e32 v72, 1.0, v73
	v_add_f32_e32 v73, 1.0, v82
	v_pk_mul_f32 v[82:83], v[6:7], v[78:79]
	v_rcp_f32_e32 v72, v72
	v_pk_fma_f32 v[76:77], v[4:5], v[76:77], v[82:83]
	v_lshlrev_b32_e32 v82, 16, v113
	v_and_b32_e32 v83, 0xffff0000, v113
	v_pk_fma_f32 v[76:77], v[70:71], v[80:81], v[76:77]
	v_rcp_f32_e32 v73, v73
	v_pk_fma_f32 v[76:77], v[68:69], v[82:83], v[76:77]
	v_pk_fma_f32 v[78:79], v[4:5], v[78:79], v[86:87]
	v_mul_f32_e32 v84, 0xbfb8aa3b, v76
	v_mul_f32_e32 v85, 0xbfb8aa3b, v77
	v_exp_f32_e32 v84, v84
	v_exp_f32_e32 v85, v85
	v_pk_mul_f32 v[72:73], v[74:75], v[72:73]
	v_pk_fma_f32 v[78:79], v[70:71], v[82:83], v[78:79]
	v_add_f32_e32 v84, 1.0, v84
	v_add_f32_e32 v85, 1.0, v85
	v_rcp_f32_e32 v84, v84
	v_rcp_f32_e32 v85, v85
	v_mul_f32_e32 v74, v73, v73
	v_pk_fma_f32 v[90:91], v[72:73], v[72:73], v[74:75] op_sel_hi:[1,1,0]
	v_pk_mul_f32 v[94:95], v[6:7], v[82:83]
	v_pk_mul_f32 v[74:75], v[76:77], v[84:85]
	v_lshlrev_b32_e32 v84, 16, v114
	v_and_b32_e32 v85, 0xffff0000, v114
	v_pk_fma_f32 v[78:79], v[68:69], v[84:85], v[78:79]
	v_mul_f32_e32 v76, v75, v75
	v_mul_f32_e32 v77, 0xbfb8aa3b, v78
	v_mul_f32_e32 v86, 0xbfb8aa3b, v79
	v_exp_f32_e32 v77, v77
	v_exp_f32_e32 v86, v86
	v_pk_fma_f32 v[80:81], v[4:5], v[80:81], v[94:95]
	v_and_b32_e32 v87, 0xffff0000, v115
	v_pk_fma_f32 v[92:93], v[74:75], v[74:75], v[76:77] op_sel_hi:[1,1,0]
	v_add_f32_e32 v76, 1.0, v77
	v_add_f32_e32 v77, 1.0, v86
	v_lshlrev_b32_e32 v86, 16, v115
	v_pk_fma_f32 v[80:81], v[70:71], v[84:85], v[80:81]
	v_rcp_f32_e32 v76, v76
	v_pk_fma_f32 v[80:81], v[68:69], v[86:87], v[80:81]
	v_rcp_f32_e32 v77, v77
	v_mul_f32_e32 v89, 0xbfb8aa3b, v80
	v_exp_f32_e32 v89, v89
	v_mul_f32_e32 v91, 0xbfb8aa3b, v81
	v_exp_f32_e32 v91, v91
	v_pk_mul_f32 v[78:79], v[78:79], v[76:77]
	v_add_f32_e32 v89, 1.0, v89
	v_rcp_f32_e32 v94, v89
	v_add_f32_e32 v89, 1.0, v91
	v_rcp_f32_e32 v95, v89
	v_pk_mul_f32 v[98:99], v[6:7], v[84:85]
	v_mul_f32_e32 v76, v79, v79
	v_pk_fma_f32 v[82:83], v[4:5], v[82:83], v[98:99]
	v_pk_fma_f32 v[96:97], v[78:79], v[78:79], v[76:77] op_sel_hi:[1,1,0]
	v_pk_mul_f32 v[76:77], v[80:81], v[94:95]
	v_lshlrev_b32_e32 v94, 16, v116
	v_and_b32_e32 v95, 0xffff0000, v116
	v_pk_fma_f32 v[82:83], v[70:71], v[86:87], v[82:83]
	v_pk_mul_f32 v[102:103], v[6:7], v[86:87]
	v_pk_fma_f32 v[82:83], v[68:69], v[94:95], v[82:83]
	v_pk_fma_f32 v[84:85], v[4:5], v[84:85], v[102:103]
	v_mul_f32_e32 v81, 0xbfb8aa3b, v82
	v_mul_f32_e32 v89, 0xbfb8aa3b, v83
	v_exp_f32_e32 v81, v81
	v_exp_f32_e32 v89, v89
	v_pk_fma_f32 v[84:85], v[70:71], v[94:95], v[84:85]
	v_mul_f32_e32 v80, v77, v77
	v_pk_fma_f32 v[84:85], v[68:69], v[100:101], v[84:85]
	v_pk_fma_f32 v[98:99], v[76:77], v[76:77], v[80:81] op_sel_hi:[1,1,0]
	v_add_f32_e32 v80, 1.0, v81
	v_add_f32_e32 v81, 1.0, v89
	v_mul_f32_e32 v89, 0xbfb8aa3b, v84
	v_exp_f32_e32 v89, v89
	v_mul_f32_e32 v91, 0xbfb8aa3b, v85
	v_exp_f32_e32 v91, v91
	v_rcp_f32_e32 v80, v80
	v_rcp_f32_e32 v81, v81
	v_add_f32_e32 v89, 1.0, v89
	v_rcp_f32_e32 v102, v89
	v_add_f32_e32 v89, 1.0, v91
	v_rcp_f32_e32 v103, v89
; DI float bflo(unsigned u) { return __uint_as_float(u << 16); }
; DI float bfhi(unsigned u) { return __uint_as_float(u & 0xffff0000u); }
; DI float swap32sum(float a, float b) { const auto r = __builtin_amdgcn_permlane32_swap(__float_as_uint(a), __float_as_uint(b), false, false); return __uint_as_float(r[0]) + __uint_as_float(r[1]); }
; DI float swap16sum(float a, float b) { const auto r = __builtin_amdgcn_permlane16_swap(__float_as_uint(a), __float_as_uint(b), false, false); return __uint_as_float(r[0]) + __uint_as_float(r[1]); }
; DI float sigmoidf_(float x) { return __builtin_amdgcn_rcpf(1.f + __expf(-x)); }
; DI void gdn_prep_unit(const Params& p, int U, char* lds) {
;     ...
;       for (int ii = 0; ii < 16; ++ii) {
;         float a0 = w0[0] * bflo(raw[ii]) + w0[1] * bflo(raw[ii + 1]) + w0[2] * bflo(raw[ii + 2]) + w0[3] * bflo(raw[ii + 3]);
;         float a1 = w1[0] * bfhi(raw[ii]) + w1[1] * bfhi(raw[ii + 1]) + w1[2] * bfhi(raw[ii + 2]) + w1[3] * bfhi(raw[ii + 3]);
;         a0 = a0 * sigmoidf_(a0); a1 = a1 * sigmoidf_(a1);
;         y0[ii] = a0; y1[ii] = a1; ssr[ii] = a0 * a0 + a1 * a1;
;       }
;       if (X < 2) {
;         const bool b3 = (lane & 8) != 0, b2 = (lane & 4) != 0;
;         float r8[8], r4[4], r2[2];
; #pragma unroll
;         for (int j = 0; j < 8; ++j) r8[j] = swap32sum(ssr[j], ssr[8 + j]);
; #pragma unroll
;         for (int j = 0; j < 4; ++j) r4[j] = swap16sum(r8[j], r8[4 + j]);
; #pragma unroll
	v_pk_mul_f32 v[80:81], v[82:83], v[80:81]
	v_pk_mul_f32 v[108:109], v[6:7], v[94:95]
	v_mul_f32_e32 v82, v81, v81
	v_pk_fma_f32 v[86:87], v[4:5], v[86:87], v[108:109]
	v_pk_fma_f32 v[106:107], v[80:81], v[80:81], v[82:83] op_sel_hi:[1,1,0]
	v_pk_mul_f32 v[82:83], v[84:85], v[102:103]
	v_lshlrev_b32_e32 v102, 16, v9
	v_and_b32_e32 v103, 0xffff0000, v9
	v_pk_fma_f32 v[86:87], v[70:71], v[100:101], v[86:87]
	v_pk_mul_f32 v[114:115], v[6:7], v[100:101]
	v_pk_fma_f32 v[86:87], v[68:69], v[102:103], v[86:87]
	v_pk_fma_f32 v[94:95], v[4:5], v[94:95], v[114:115]
	v_mul_f32_e32 v9, 0xbfb8aa3b, v86
	v_exp_f32_e32 v9, v9
	v_mul_f32_e32 v85, 0xbfb8aa3b, v87
	v_exp_f32_e32 v85, v85
	v_and_b32_e32 v113, 0xffff0000, v37
	v_pk_fma_f32 v[94:95], v[70:71], v[102:103], v[94:95]
	v_mul_f32_e32 v84, v83, v83
	v_pk_fma_f32 v[94:95], v[68:69], v[112:113], v[94:95]
	v_add_f32_e32 v9, 1.0, v9
	v_mul_f32_e32 v37, 0xbfb8aa3b, v94
	v_pk_fma_f32 v[108:109], v[82:83], v[82:83], v[84:85] op_sel_hi:[1,1,0]
	v_rcp_f32_e32 v84, v9
	v_add_f32_e32 v9, 1.0, v85
	v_exp_f32_e32 v37, v37
	v_mul_f32_e32 v85, 0xbfb8aa3b, v95
	v_exp_f32_e32 v89, v85
	v_rcp_f32_e32 v85, v9
	v_add_f32_e32 v9, 1.0, v37
	v_rcp_f32_e32 v114, v9
	v_add_f32_e32 v9, 1.0, v89
	v_rcp_f32_e32 v115, v9
	v_pk_mul_f32 v[86:87], v[86:87], v[84:85]
	v_pk_mul_f32 v[120:121], v[6:7], v[102:103]
	v_mul_f32_e32 v84, v87, v87
	v_pk_fma_f32 v[100:101], v[4:5], v[100:101], v[120:121]
	v_pk_fma_f32 v[118:119], v[86:87], v[86:87], v[84:85] op_sel_hi:[1,1,0]
	v_pk_mul_f32 v[84:85], v[94:95], v[114:115]
	v_lshlrev_b32_e32 v114, 16, v104
	v_and_b32_e32 v115, 0xffff0000, v104
	v_pk_fma_f32 v[100:101], v[70:71], v[112:113], v[100:101]
	v_mul_f32_e32 v94, v85, v85
	v_pk_fma_f32 v[100:101], v[68:69], v[114:115], v[100:101]
	v_pk_fma_f32 v[94:95], v[84:85], v[84:85], v[94:95] op_sel_hi:[1,1,0]
	v_mul_f32_e32 v9, 0xbfb8aa3b, v100
	v_exp_f32_e32 v9, v9
	v_mul_f32_e32 v37, 0xbfb8aa3b, v101
	v_exp_f32_e32 v37, v37
	v_permlane32_swap_b32_e32 v88, v94
	v_add_f32_e32 v9, 1.0, v9
	v_rcp_f32_e32 v120, v9
	v_add_f32_e32 v9, 1.0, v37
	v_rcp_f32_e32 v121, v9
	v_add_f32_e32 v9, v88, v94
	v_pk_mul_f32 v[88:89], v[100:101], v[120:121]
	v_pk_mul_f32 v[120:121], v[6:7], v[112:113]
	v_lshlrev_b32_e32 v100, 16, v110
	v_pk_fma_f32 v[102:103], v[4:5], v[102:103], v[120:121]
	v_and_b32_e32 v101, 0xffff0000, v110
	v_pk_fma_f32 v[102:103], v[70:71], v[114:115], v[102:103]
	v_mul_f32_e32 v94, v89, v89
	v_pk_fma_f32 v[102:103], v[68:69], v[100:101], v[102:103]
	v_pk_fma_f32 v[94:95], v[88:89], v[88:89], v[94:95] op_sel_hi:[1,1,0]
	v_mul_f32_e32 v37, 0xbfb8aa3b, v102
	v_exp_f32_e32 v37, v37
	v_mul_f32_e32 v91, 0xbfb8aa3b, v103
	v_exp_f32_e32 v91, v91
	v_permlane32_swap_b32_e32 v90, v94
	v_add_f32_e32 v37, 1.0, v37
	v_rcp_f32_e32 v120, v37
	v_add_f32_e32 v37, 1.0, v91
	v_rcp_f32_e32 v121, v37
	v_add_f32_e32 v37, v90, v94
	v_pk_mul_f32 v[90:91], v[102:103], v[120:121]
	v_pk_mul_f32 v[120:121], v[6:7], v[114:115]
	v_lshlrev_b32_e32 v102, 16, v122
	v_pk_fma_f32 v[112:113], v[4:5], v[112:113], v[120:121]
	v_and_b32_e32 v103, 0xffff0000, v122
	v_pk_fma_f32 v[112:113], v[70:71], v[100:101], v[112:113]
	v_mul_f32_e32 v94, v91, v91
	v_pk_fma_f32 v[112:113], v[68:69], v[102:103], v[112:113]
	s_nop 0
	v_mul_f32_e32 v93, 0xbfb8aa3b, v112
	v_exp_f32_e32 v93, v93
	v_mul_f32_e32 v95, 0xbfb8aa3b, v113
	v_exp_f32_e32 v97, v95
	v_pk_fma_f32 v[94:95], v[90:91], v[90:91], v[94:95] op_sel_hi:[1,1,0]
	v_add_f32_e32 v93, 1.0, v93
	v_rcp_f32_e32 v120, v93
	v_add_f32_e32 v93, 1.0, v97
	v_rcp_f32_e32 v121, v93
	v_permlane32_swap_b32_e32 v92, v94
	v_add_f32_e32 v104, v92, v94
	v_pk_mul_f32 v[92:93], v[112:113], v[120:121]
	v_pk_mul_f32 v[120:121], v[6:7], v[100:101]
	v_lshlrev_b32_e32 v112, 16, v124
	v_pk_fma_f32 v[114:115], v[4:5], v[114:115], v[120:121]
	v_and_b32_e32 v113, 0xffff0000, v124
	v_pk_fma_f32 v[114:115], v[70:71], v[102:103], v[114:115]
	v_mul_f32_e32 v94, v93, v93
	v_pk_fma_f32 v[114:115], v[68:69], v[112:113], v[114:115]
	s_nop 0
	v_mul_f32_e32 v95, 0xbfb8aa3b, v114
	v_exp_f32_e32 v97, v95
	v_mul_f32_e32 v95, 0xbfb8aa3b, v115
	v_exp_f32_e32 v99, v95
	v_pk_fma_f32 v[94:95], v[92:93], v[92:93], v[94:95] op_sel_hi:[1,1,0]
	s_nop 0
	v_add_f32_e32 v95, 1.0, v97
	v_rcp_f32_e32 v120, v95
	v_add_f32_e32 v95, 1.0, v99
	v_rcp_f32_e32 v121, v95
	v_permlane32_swap_b32_e32 v96, v94
	v_add_f32_e32 v107, v96, v94
	v_pk_mul_f32 v[94:95], v[114:115], v[120:121]
	v_pk_mul_f32 v[120:121], v[6:7], v[102:103]
	v_mul_f32_e32 v96, v95, v95
	v_pk_fma_f32 v[100:101], v[4:5], v[100:101], v[120:121]
	v_lshlrev_b32_e32 v114, 16, v125
	v_and_b32_e32 v115, 0xffff0000, v125
	v_pk_fma_f32 v[100:101], v[70:71], v[112:113], v[100:101]
	v_pk_fma_f32 v[96:97], v[94:95], v[94:95], v[96:97] op_sel_hi:[1,1,0]
	v_pk_fma_f32 v[100:101], v[68:69], v[114:115], v[100:101]
	s_nop 0
	v_permlane32_swap_b32_e32 v98, v96
	v_mul_f32_e32 v97, 0xbfb8aa3b, v100
	v_mul_f32_e32 v99, 0xbfb8aa3b, v101
	v_exp_f32_e32 v97, v97
	v_exp_f32_e32 v99, v99
	v_add_f32_e32 v98, v98, v96
	v_pk_mul_f32 v[120:121], v[6:7], v[112:113]
	v_add_f32_e32 v96, 1.0, v97
	v_add_f32_e32 v97, 1.0, v99
	v_rcp_f32_e32 v96, v96
	v_rcp_f32_e32 v97, v97
	v_permlane16_swap_b32_e32 v9, v98
	v_pk_fma_f32 v[102:103], v[4:5], v[102:103], v[120:121]
	v_pk_mul_f32 v[96:97], v[100:101], v[96:97]
	v_add_f32_e32 v9, v9, v98
	v_mul_f32_e32 v98, v97, v97
	v_lshlrev_b32_e32 v100, 16, v126
	v_and_b32_e32 v101, 0xffff0000, v126
	v_pk_fma_f32 v[102:103], v[70:71], v[114:115], v[102:103]
	v_pk_fma_f32 v[98:99], v[96:97], v[96:97], v[98:99] op_sel_hi:[1,1,0]
	v_pk_fma_f32 v[102:103], v[68:69], v[100:101], v[102:103]
	s_nop 0
	v_permlane32_swap_b32_e32 v106, v98
; DI unsigned pk2(float lo, float hi) { f32x2 v = {lo, hi}; bf16x2_t b = __builtin_convertvector(v, bf16x2_t); return __builtin_bit_cast(unsigned, b); }
; DI float dpp_xor8(float v) { return __uint_as_float((unsigned)__builtin_amdgcn_update_dpp(0, (int)__float_as_uint(v), 0x128, 0xF, 0xF, true)); }
; DI float swap32sum(float a, float b) { const auto r = __builtin_amdgcn_permlane32_swap(__float_as_uint(a), __float_as_uint(b), false, false); return __uint_as_float(r[0]) + __uint_as_float(r[1]); }
; DI float swap16sum(float a, float b) { const auto r = __builtin_amdgcn_permlane16_swap(__float_as_uint(a), __float_as_uint(b), false, false); return __uint_as_float(r[0]) + __uint_as_float(r[1]); }
; DI void gdn_prep_unit(const Params& p, int U, char* lds) {
;     ...
;         for (int j = 0; j < 8; ++j) r8[j] = swap32sum(ssr[j], ssr[8 + j]);
; #pragma unroll
;         for (int j = 0; j < 4; ++j) r4[j] = swap16sum(r8[j], r8[4 + j]);
; #pragma unroll
;         for (int j = 0; j < 2; ++j) { const float keep = b3 ? r4[2 + j] : r4[j], send = b3 ? r4[j] : r4[2 + j]; r2[j] = keep + dpp_xor8(send); }
;         float r1 = (b2 ? r2[1] : r2[0]) + __shfl_xor(b2 ? r2[0] : r2[1], 4);
;         r1 += __uint_as_float((unsigned)__builtin_amdgcn_update_dpp(0, (int)__float_as_uint(r1), 0x4E, 0xF, 0xF, true));
;         r1 += __uint_as_float((unsigned)__builtin_amdgcn_update_dpp(0, (int)__float_as_uint(r1), 0xB1, 0xF, 0xF, true));
; #pragma unroll
;         for (int ii = 0; ii < 16; ++ii) ssr[ii] = __uint_as_float((unsigned)__builtin_amdgcn_readlane((int)__float_as_uint(r1), 4 * ii));
;       }
; #pragma unroll
;       for (int ii = 0; ii < 16; ++ii) {
;         const int i = i0 + ii;
;         float a0 = y0[ii], a1 = y1[ii];
;         if (X < 2) { const float rn = rsqrtf(ssr[ii] + 1e-6f); a0 *= rn; a1 *= rn; }
;         *(unsigned*)(dst + i * QP + 2 * lane) = pk2(a0, a1);
	v_mul_f32_e32 v99, 0xbfb8aa3b, v102
	v_mul_f32_e32 v109, 0xbfb8aa3b, v103
	v_exp_f32_e32 v99, v99
	v_exp_f32_e32 v109, v109
	v_add_f32_e32 v106, v106, v98
	v_pk_mul_f32 v[6:7], v[6:7], v[114:115]
	v_add_f32_e32 v98, 1.0, v99
	v_add_f32_e32 v99, 1.0, v109
	v_rcp_f32_e32 v98, v98
	v_rcp_f32_e32 v99, v99
	v_permlane16_swap_b32_e32 v37, v106
	v_pk_fma_f32 v[4:5], v[4:5], v[112:113], v[6:7]
	v_pk_mul_f32 v[98:99], v[102:103], v[98:99]
	v_add_f32_e32 v37, v37, v106
	v_mul_f32_e32 v102, v99, v99
	v_pk_fma_f32 v[102:103], v[98:99], v[98:99], v[102:103] op_sel_hi:[1,1,0]
	v_pk_fma_f32 v[4:5], v[70:71], v[100:101], v[4:5]
	s_nop 0
	v_permlane32_swap_b32_e32 v108, v102
	v_add_f32_e32 v106, v108, v102
	v_lshlrev_b32_e32 v102, 16, v127
	v_and_b32_e32 v103, 0xffff0000, v127
	v_pk_fma_f32 v[4:5], v[68:69], v[102:103], v[4:5]
	v_permlane16_swap_b32_e32 v104, v106
	v_mul_f32_e32 v6, 0xbfb8aa3b, v4
	v_mul_f32_e32 v7, 0xbfb8aa3b, v5
	v_exp_f32_e32 v6, v6
	v_exp_f32_e32 v7, v7
	v_add_f32_e32 v68, v104, v106
	v_cndmask_b32_e64 v69, v68, v9, s[0:1]
	v_add_f32_e32 v6, 1.0, v6
	v_add_f32_e32 v7, 1.0, v7
	v_rcp_f32_e32 v6, v6
	v_rcp_f32_e32 v7, v7
	v_cndmask_b32_e64 v9, v9, v68, s[0:1]
	s_nop 1
	v_add_f32_dpp v9, v9, v69 row_ror:8 row_mask:0xf bank_mask:0xf bound_ctrl:1
	v_pk_mul_f32 v[68:69], v[4:5], v[6:7]
	s_nop 0
	v_mul_f32_e32 v4, v69, v69
	v_pk_fma_f32 v[4:5], v[68:69], v[68:69], v[4:5] op_sel_hi:[1,1,0]
	s_nop 1
	v_permlane32_swap_b32_e32 v118, v4
	v_add_f32_e32 v4, v118, v4
	s_nop 1
	v_permlane16_swap_b32_e32 v107, v4
	v_add_f32_e32 v4, v107, v4
	v_cndmask_b32_e64 v5, v4, v37, s[0:1]
	v_cndmask_b32_e64 v4, v37, v4, s[0:1]
	s_nop 1
	v_add_f32_dpp v4, v4, v5 row_ror:8 row_mask:0xf bank_mask:0xf bound_ctrl:1
	v_cndmask_b32_e64 v5, v9, v4, s[12:13]
	ds_bpermute_b32 v5, v55, v5
	v_cndmask_b32_e64 v4, v4, v9, s[12:13]
	v_and_b32_e32 v55, 15, v175
	s_waitcnt lgkmcnt(0)
	v_add_f32_e32 v4, v4, v5
	s_nop 1
	v_add_f32_dpp v4, v4, v4 quad_perm:[2,3,0,1] row_mask:0xf bank_mask:0xf bound_ctrl:1
	s_nop 1
	v_add_f32_dpp v6, v4, v4 quad_perm:[1,0,3,2] row_mask:0xf bank_mask:0xf bound_ctrl:1
	s_nop 0
	v_readlane_b32 s1, v6, 0
	v_readlane_b32 s0, v6, 4
	v_readlane_b32 s13, v6, 8
	v_readlane_b32 s12, v6, 12
	v_pk_add_f32 v[4:5], s[0:1], v[32:33] op_sel_hi:[1,0]
	v_readlane_b32 s75, v6, 16
	v_mul_f32_e32 v7, 0x4b800000, v5
	v_cmp_gt_f32_e64 s[0:1], s19, v5
	v_readlane_b32 s74, v6, 20
	v_readlane_b32 s61, v6, 24
	v_cndmask_b32_e64 v5, v5, v7, s[0:1]
	v_rsq_f32_e32 v5, v5
	v_readlane_b32 s60, v6, 28
	v_readlane_b32 s51, v6, 32
	v_readlane_b32 s50, v6, 36
	v_readlane_b32 s49, v6, 40
	v_readlane_b32 s48, v6, 44
	v_readlane_b32 s45, v6, 48
	v_readlane_b32 s44, v6, 52
	v_readlane_b32 s15, v6, 56
	v_readlane_b32 s14, v6, 60
	v_mul_f32_e32 v6, 0x45800000, v5
	v_cndmask_b32_e64 v6, v5, v6, s[0:1]
	v_mul_f32_e32 v5, 0x4b800000, v4
	v_cmp_gt_f32_e64 s[0:1], s19, v4
	s_nop 1
	v_cndmask_b32_e64 v4, v4, v5, s[0:1]
	v_rsq_f32_e32 v7, v4
	s_nop 0
	v_pk_mul_f32 v[4:5], v[6:7], v[66:67] op_sel_hi:[0,1]
	v_cvt_pk_bf16_f32 v4, v4, v5
	ds_write_b32 v8, v4 offset:17408
	v_pk_add_f32 v[4:5], s[12:13], v[32:33] op_sel_hi:[1,0]
	v_mul_f32_e32 v6, 0x45800000, v7
	v_mul_f32_e32 v9, 0x4b800000, v5
	v_cmp_gt_f32_e64 s[12:13], s19, v5
	v_cndmask_b32_e64 v6, v7, v6, s[0:1]
	v_pk_mul_f32 v[6:7], v[6:7], v[72:73] op_sel_hi:[0,1]
	v_cndmask_b32_e64 v5, v5, v9, s[12:13]
	v_rsq_f32_e32 v5, v5
	v_cvt_pk_bf16_f32 v9, v6, v7
	v_cmp_gt_f32_e64 s[0:1], s19, v4
	v_add_u32_e32 v66, 0x4400, v36
	v_mul_f32_e32 v6, 0x45800000, v5
	v_cndmask_b32_e64 v6, v5, v6, s[12:13]
	v_mul_f32_e32 v5, 0x4b800000, v4
	v_pk_mul_f32 v[6:7], v[6:7], v[74:75] op_sel_hi:[0,1]
	v_cndmask_b32_e64 v4, v4, v5, s[0:1]
	v_rsq_f32_e32 v37, v4
	v_cvt_pk_bf16_f32 v4, v6, v7
	ds_write2_b32 v66, v9, v4 offset1:68
	v_pk_add_f32 v[4:5], s[74:75], v[32:33] op_sel_hi:[1,0]
	v_mul_f32_e32 v6, 0x45800000, v37
	v_mul_f32_e32 v7, 0x4b800000, v5
	v_cmp_gt_f32_e64 s[12:13], s19, v5
	v_cndmask_b32_e64 v6, v37, v6, s[0:1]
	v_cmp_gt_f32_e64 s[0:1], s19, v4
	v_cndmask_b32_e64 v5, v5, v7, s[12:13]
	v_rsq_f32_e32 v5, v5
	v_pk_mul_f32 v[6:7], v[6:7], v[78:79] op_sel_hi:[0,1]
	v_cvt_pk_bf16_f32 v7, v6, v7
	v_mul_f32_e32 v6, 0x45800000, v5
	v_cndmask_b32_e64 v6, v5, v6, s[12:13]
	v_mul_f32_e32 v5, 0x4b800000, v4
	v_cndmask_b32_e64 v4, v4, v5, s[0:1]
	v_rsq_f32_e32 v9, v4
	v_pk_mul_f32 v[4:5], v[6:7], v[76:77] op_sel_hi:[0,1]
	v_cvt_pk_bf16_f32 v4, v4, v5
	ds_write2_b32 v66, v7, v4 offset0:136 offset1:204
	v_pk_add_f32 v[4:5], s[60:61], v[32:33] op_sel_hi:[1,0]
	v_mul_f32_e32 v6, 0x45800000, v9
	v_mul_f32_e32 v7, 0x4b800000, v5
	v_cmp_gt_f32_e64 s[12:13], s19, v5
	v_cndmask_b32_e64 v6, v9, v6, s[0:1]
	v_cmp_gt_f32_e64 s[0:1], s19, v4
	v_cndmask_b32_e64 v5, v5, v7, s[12:13]
	v_rsq_f32_e32 v5, v5
	v_pk_mul_f32 v[6:7], v[6:7], v[80:81] op_sel_hi:[0,1]
	v_cvt_pk_bf16_f32 v9, v6, v7
	v_add_u32_e32 v66, 0x4800, v36
	v_mul_f32_e32 v6, 0x45800000, v5
	v_cndmask_b32_e64 v6, v5, v6, s[12:13]
	v_mul_f32_e32 v5, 0x4b800000, v4
	v_pk_mul_f32 v[6:7], v[6:7], v[82:83] op_sel_hi:[0,1]
	v_cndmask_b32_e64 v4, v4, v5, s[0:1]
	v_rsq_f32_e32 v37, v4
	v_cvt_pk_bf16_f32 v4, v6, v7
	ds_write2_b32 v66, v9, v4 offset0:16 offset1:84
	v_pk_add_f32 v[4:5], s[50:51], v[32:33] op_sel_hi:[1,0]
	v_mul_f32_e32 v6, 0x45800000, v37
	v_mul_f32_e32 v7, 0x4b800000, v5
	v_cmp_gt_f32_e64 s[12:13], s19, v5
	v_cndmask_b32_e64 v6, v37, v6, s[0:1]
	v_cmp_gt_f32_e64 s[0:1], s19, v4
	v_cndmask_b32_e64 v5, v5, v7, s[12:13]
	v_rsq_f32_e32 v5, v5
	v_pk_mul_f32 v[6:7], v[6:7], v[86:87] op_sel_hi:[0,1]
	v_cvt_pk_bf16_f32 v7, v6, v7
	v_mul_f32_e32 v6, 0x45800000, v5
	v_cndmask_b32_e64 v6, v5, v6, s[12:13]
; DI void gdn_prep_unit(const Params& p, int U, char* lds) {
;     ...
;     for (int X = 0; X < 3; ++X) {
;       const int col = 1536 + 512 * X + h * 128 + 2 * lane, cb = 512 * X + h * 128 + 2 * lane;
;       float w0[4], w1[4];
; #pragma unroll
;       for (int j = 0; j < 4; ++j) { w0[j] = p.conv_w[j * 1536 + cb]; w1[j] = p.conv_w[j * 1536 + cb + 1]; }
;       bf16_t* dst = X == 0 ? q_s : (X == 1 ? k_s : v_s);
;       const int i0 = 16 * wid;
;       unsigned raw[19];
;       {
;         const unsigned* pr[19];
; #pragma unroll
;         for (int j = 0; j < 19; ++j) { const int rr = i0 - 3 + j; const int rc = (s0 + rr >= 0) ? rr : -s0;
;           pr[j] = (const unsigned*)(proj + (size_t)((long)t0 + rc) * PP + col); }
;         asm volatile("global_load_dword %0, %10, off\n\tglobal_load_dword %1, %11, off\n\tglobal_load_dword %2, %12, off\n\tglobal_load_dword %3, %13, off\n\tglobal_load_dword %4, %14, off\n\t"
;                      "global_load_dword %5, %15, off\n\tglobal_load_dword %6, %16, off\n\tglobal_load_dword %7, %17, off\n\tglobal_load_dword %8, %18, off\n\tglobal_load_dword %9, %19, off\n\ts_waitcnt vmcnt(0)"
;                      : "=&v"(raw[0]), "=&v"(raw[1]), "=&v"(raw[2]), "=&v"(raw[3]), "=&v"(raw[4]), "=&v"(raw[5]), "=&v"(raw[6]), "=&v"(raw[7]), "=&v"(raw[8]), "=&v"(raw[9])
;                      : "v"(pr[0]), "v"(pr[1]), "v"(pr[2]), "v"(pr[3]), "v"(pr[4]), "v"(pr[5]), "v"(pr[6]), "v"(pr[7]), "v"(pr[8]), "v"(pr[9]) : "memory");
;         asm volatile("global_load_dword %0, %9, off\n\tglobal_load_dword %1, %10, off\n\tglobal_load_dword %2, %11, off\n\tglobal_load_dword %3, %12, off\n\tglobal_load_dword %4, %13, off\n\t"
;                      "global_load_dword %5, %14, off\n\tglobal_load_dword %6, %15, off\n\tglobal_load_dword %7, %16, off\n\tglobal_load_dword %8, %17, off\n\ts_waitcnt vmcnt(0)"
;                      : "=&v"(raw[10]), "=&v"(raw[11]), "=&v"(raw[12]), "=&v"(raw[13]), "=&v"(raw[14]), "=&v"(raw[15]), "=&v"(raw[16]), "=&v"(raw[17]), "=&v"(raw[18])
;     ...
;       for (int ii = 0; ii < 16; ++ii) {
;         const int i = i0 + ii;
;         float a0 = y0[ii], a1 = y1[ii];
;         if (X < 2) { const float rn = rsqrtf(ssr[ii] + 1e-6f); a0 *= rn; a1 *= rn; }
;         *(unsigned*)(dst + i * QP + 2 * lane) = pk2(a0, a1);
	v_mul_f32_e32 v5, 0x4b800000, v4
	v_cndmask_b32_e64 v4, v4, v5, s[0:1]
	v_rsq_f32_e32 v9, v4
	v_pk_mul_f32 v[4:5], v[6:7], v[84:85] op_sel_hi:[0,1]
	v_cvt_pk_bf16_f32 v4, v4, v5
	ds_write2_b32 v66, v7, v4 offset0:152 offset1:220
	v_pk_add_f32 v[4:5], s[48:49], v[32:33] op_sel_hi:[1,0]
	v_mul_f32_e32 v6, 0x45800000, v9
	v_mul_f32_e32 v7, 0x4b800000, v5
	v_cmp_gt_f32_e64 s[12:13], s19, v5
	v_cndmask_b32_e64 v6, v9, v6, s[0:1]
	v_cmp_gt_f32_e64 s[0:1], s19, v4
	v_cndmask_b32_e64 v5, v5, v7, s[12:13]
	v_rsq_f32_e32 v5, v5
	v_pk_mul_f32 v[6:7], v[6:7], v[88:89] op_sel_hi:[0,1]
	v_cvt_pk_bf16_f32 v9, v6, v7
	v_add_u32_e32 v66, 0x4c00, v36
	v_mul_f32_e32 v6, 0x45800000, v5
	v_cndmask_b32_e64 v6, v5, v6, s[12:13]
	v_mul_f32_e32 v5, 0x4b800000, v4
	v_pk_mul_f32 v[6:7], v[6:7], v[90:91] op_sel_hi:[0,1]
	v_cndmask_b32_e64 v4, v4, v5, s[0:1]
	v_rsq_f32_e32 v37, v4
	v_cvt_pk_bf16_f32 v4, v6, v7
	ds_write2_b32 v66, v9, v4 offset0:32 offset1:100
	v_pk_add_f32 v[4:5], s[44:45], v[32:33] op_sel_hi:[1,0]
	v_mul_f32_e32 v6, 0x45800000, v37
	v_mul_f32_e32 v7, 0x4b800000, v5
	v_cmp_gt_f32_e64 s[12:13], s19, v5
	v_cndmask_b32_e64 v6, v37, v6, s[0:1]
	v_cmp_gt_f32_e64 s[0:1], s19, v4
	v_cndmask_b32_e64 v5, v5, v7, s[12:13]
	v_rsq_f32_e32 v5, v5
	v_pk_mul_f32 v[6:7], v[6:7], v[92:93] op_sel_hi:[0,1]
	v_cvt_pk_bf16_f32 v7, v6, v7
	v_mul_f32_e32 v6, 0x45800000, v5
	v_cndmask_b32_e64 v6, v5, v6, s[12:13]
	v_mul_f32_e32 v5, 0x4b800000, v4
	v_cndmask_b32_e64 v4, v4, v5, s[0:1]
	v_rsq_f32_e32 v9, v4
	v_pk_mul_f32 v[4:5], v[94:95], v[6:7] op_sel_hi:[1,0]
	v_mul_f32_e32 v6, 0x45800000, v9
	v_cvt_pk_bf16_f32 v4, v4, v5
	ds_write2_b32 v66, v7, v4 offset0:168 offset1:236
	v_pk_add_f32 v[4:5], s[14:15], v[32:33] op_sel_hi:[1,0]
	v_cndmask_b32_e64 v6, v9, v6, s[0:1]
	v_mul_f32_e32 v7, 0x4b800000, v5
	v_cmp_gt_f32_e64 s[12:13], s19, v5
	v_cmp_gt_f32_e64 s[0:1], s19, v4
	s_nop 0
	v_cndmask_b32_e64 v5, v5, v7, s[12:13]
	v_rsq_f32_e32 v5, v5
	v_pk_mul_f32 v[6:7], v[96:97], v[6:7] op_sel_hi:[1,0]
	s_nop 0
	v_cvt_pk_bf16_f32 v9, v6, v7
	v_mul_f32_e32 v6, 0x45800000, v5
	v_cndmask_b32_e64 v6, v5, v6, s[12:13]
	v_pk_mul_f32 v[6:7], v[98:99], v[6:7] op_sel_hi:[1,0]
	v_mul_f32_e32 v5, 0x4b800000, v4
	v_cvt_pk_bf16_f32 v6, v6, v7
	v_cndmask_b32_e64 v7, v4, v5, s[0:1]
	global_load_dwordx2 v[4:5], v[64:65], off
	s_nop 0
	global_load_dwordx2 v[2:3], v[2:3], off offset:2048
	v_rsq_f32_e32 v37, v7
	v_add_u32_e32 v7, 0x5000, v36
	ds_write2_b32 v7, v9, v6 offset0:48 offset1:116
	global_load_dwordx2 v[6:7], v[56:57], off
	v_mul_f32_e32 v9, 0x45800000, v37
	global_load_dwordx2 v[0:1], v[0:1], off offset:2048
	v_cndmask_b32_e64 v56, v37, v9, s[0:1]
	s_mov_b64 s[0:1], 0x1400
	v_pk_mul_f32 v[56:57], v[68:69], v[56:57] op_sel_hi:[1,0]
	v_lshl_add_u64 v[10:11], v[10:11], 0, s[0:1]
	v_cvt_pk_bf16_f32 v9, v56, v57
	v_mad_u64_u32 v[56:57], s[0:1], v12, s3, v[10:11]
	v_add_u32_e32 v57, v13, v57
	v_mad_u64_u32 v[12:13], s[0:1], v14, s3, v[10:11]
	v_add_u32_e32 v13, v15, v13
	v_mad_u64_u32 v[14:15], s[0:1], v16, s3, v[10:11]
	v_add_u32_e32 v15, v17, v15
	v_mad_u64_u32 v[16:17], s[0:1], v18, s3, v[10:11]
	v_add_u32_e32 v17, v19, v17
	v_mad_u64_u32 v[18:19], s[0:1], v20, s3, v[10:11]
	v_add_u32_e32 v19, v21, v19
	v_mad_u64_u32 v[20:21], s[0:1], v22, s3, v[10:11]
	v_add_u32_e32 v21, v23, v21
	v_mad_u64_u32 v[22:23], s[0:1], v24, s3, v[10:11]
	v_add_u32_e32 v23, v25, v23
	v_mad_u64_u32 v[24:25], s[0:1], v38, s3, v[10:11]
	ds_write_b32 v36, v9 offset:21216
	v_add_u32_e32 v25, v39, v25
	v_mad_u64_u32 v[38:39], s[0:1], v40, s3, v[10:11]
	v_mad_u64_u32 v[64:65], s[0:1], v42, s3, v[10:11]
	v_mad_u64_u32 v[66:67], s[0:1], v44, s3, v[10:11]
	v_mad_u64_u32 v[76:77], s[0:1], v58, s3, v[10:11]
	v_add_u32_e32 v39, v193, v39
	v_add_u32_e32 v65, v194, v65
	v_add_u32_e32 v67, v45, v67
	v_mad_u64_u32 v[44:45], s[0:1], v46, s3, v[10:11]
	v_mad_u64_u32 v[68:69], s[0:1], v48, s3, v[10:11]
	v_mad_u64_u32 v[70:71], s[0:1], v50, s3, v[10:11]
	v_mad_u64_u32 v[72:73], s[0:1], v52, s3, v[10:11]
	v_mad_u64_u32 v[74:75], s[0:1], v54, s3, v[10:11]
	v_add_u32_e32 v77, v59, v77
	v_mad_u64_u32 v[58:59], s[0:1], v60, s3, v[10:11]
	v_mov_b32_e32 v9, v231
	v_mov_b32_e32 v37, v232
	v_mov_b32_e32 v40, v233
	v_mov_b32_e32 v42, v234
	v_mov_b32_e32 v46, v235
	v_mov_b32_e32 v48, v236
	v_mov_b32_e32 v50, v237
	v_mov_b32_e32 v52, v238
	v_mov_b32_e32 v54, v239
	v_mov_b32_e32 v60, v240
	s_waitcnt vmcnt(0)
	v_mad_u64_u32 v[10:11], s[0:1], v62, s3, v[10:11]
	v_cndmask_b32_e64 v15, v37, 0, s[8:9]
	v_cndmask_b32_e64 v9, v9, 0, vcc
	v_lshlrev_b32_e32 v14, 16, v15
	v_and_b32_e32 v15, 0xffff0000, v15
	v_cndmask_b32_e64 v18, v40, 0, s[10:11]
	v_lshlrev_b32_e32 v12, 16, v9
	v_and_b32_e32 v13, 0xffff0000, v9
	v_and_b32_e32 v19, 0xffff0000, v42
	v_add_u32_e32 v45, v195, v45
	v_add_u32_e32 v69, v196, v69
	v_add_u32_e32 v71, v197, v71
	v_add_u32_e32 v73, v198, v73
	v_add_u32_e32 v75, v199, v75
	v_add_u32_e32 v59, v61, v59
	v_add_u32_e32 v11, v63, v11
	v_cmp_gt_i32_e32 vcc, 1, v181
	s_waitcnt vmcnt(2)
	v_pk_mul_f32 v[16:17], v[2:3], v[14:15]
	s_nop 0
	v_pk_fma_f32 v[12:13], v[4:5], v[12:13], v[16:17]
	v_lshlrev_b32_e32 v16, 16, v18
	v_and_b32_e32 v17, 0xffff0000, v18
	s_waitcnt vmcnt(1)
	v_pk_fma_f32 v[12:13], v[6:7], v[16:17], v[12:13]
	v_lshlrev_b32_e32 v18, 16, v42
	s_waitcnt vmcnt(0)
	v_pk_fma_f32 v[12:13], v[0:1], v[18:19], v[12:13]
	v_mov_b32_e32 v37, v241
	v_mov_b32_e32 v40, v242
	v_mov_b32_e32 v42, v243
	v_mov_b32_e32 v78, v244
	v_mov_b32_e32 v79, v245
	v_mov_b32_e32 v80, v246
	v_mov_b32_e32 v81, v247
	v_mov_b32_e32 v82, v248
	v_mov_b32_e32 v83, v249
	s_waitcnt vmcnt(0)
; DI float bflo(unsigned u) { return __uint_as_float(u << 16); }
; DI float bfhi(unsigned u) { return __uint_as_float(u & 0xffff0000u); }
; DI float sigmoidf_(float x) { return __builtin_amdgcn_rcpf(1.f + __expf(-x)); }
; DI void gdn_prep_unit(const Params& p, int U, char* lds) {
;     ...
; #pragma unroll
;       for (int ii = 0; ii < 16; ++ii) {
;         float a0 = w0[0] * bflo(raw[ii]) + w0[1] * bflo(raw[ii + 1]) + w0[2] * bflo(raw[ii + 2]) + w0[3] * bflo(raw[ii + 3]);
;         float a1 = w1[0] * bfhi(raw[ii]) + w1[1] * bfhi(raw[ii + 1]) + w1[2] * bfhi(raw[ii + 2]) + w1[3] * bfhi(raw[ii + 3]);
;         a0 = a0 * sigmoidf_(a0); a1 = a1 * sigmoidf_(a1);
;         y0[ii] = a0; y1[ii] = a1; ssr[ii] = a0 * a0 + a1 * a1;
;       }
	s_nop 0
	v_mul_f32_e32 v9, 0xbfb8aa3b, v12
	v_exp_f32_e32 v9, v9
	v_mul_f32_e32 v20, 0xbfb8aa3b, v13
	v_exp_f32_e32 v20, v20
	v_add_f32_e32 v9, 1.0, v9
	v_rcp_f32_e32 v10, v9
	v_add_f32_e32 v9, 1.0, v20
	v_pk_mul_f32 v[20:21], v[2:3], v[16:17]
	v_rcp_f32_e32 v11, v9
	v_pk_fma_f32 v[14:15], v[4:5], v[14:15], v[20:21]
	v_lshlrev_b32_e32 v20, 16, v46
	v_pk_fma_f32 v[14:15], v[6:7], v[18:19], v[14:15]
	v_and_b32_e32 v21, 0xffff0000, v46
	v_pk_fma_f32 v[14:15], v[0:1], v[20:21], v[14:15]
	v_pk_mul_f32 v[10:11], v[12:13], v[10:11]
	v_mul_f32_e32 v9, 0xbfb8aa3b, v14
	v_exp_f32_e32 v9, v9
	v_mul_f32_e32 v22, 0xbfb8aa3b, v15
	v_exp_f32_e32 v22, v22
	v_add_f32_e32 v9, 1.0, v9
	v_rcp_f32_e32 v12, v9
	v_add_f32_e32 v9, 1.0, v22
	v_pk_mul_f32 v[22:23], v[2:3], v[18:19]
	v_rcp_f32_e32 v13, v9
	v_pk_fma_f32 v[16:17], v[4:5], v[16:17], v[22:23]
	v_lshlrev_b32_e32 v22, 16, v48
	v_pk_fma_f32 v[16:17], v[6:7], v[20:21], v[16:17]
	v_and_b32_e32 v23, 0xffff0000, v48
	v_pk_fma_f32 v[16:17], v[0:1], v[22:23], v[16:17]
	v_pk_mul_f32 v[12:13], v[14:15], v[12:13]
	v_mul_f32_e32 v9, 0xbfb8aa3b, v16
	v_exp_f32_e32 v9, v9
	v_mul_f32_e32 v24, 0xbfb8aa3b, v17
	v_exp_f32_e32 v24, v24
	v_add_f32_e32 v9, 1.0, v9
	v_rcp_f32_e32 v14, v9
	v_add_f32_e32 v9, 1.0, v24
	v_pk_mul_f32 v[24:25], v[2:3], v[20:21]
	v_rcp_f32_e32 v15, v9
	v_pk_fma_f32 v[18:19], v[4:5], v[18:19], v[24:25]
	v_lshlrev_b32_e32 v24, 16, v50
	v_pk_fma_f32 v[18:19], v[6:7], v[22:23], v[18:19]
	v_and_b32_e32 v25, 0xffff0000, v50
	v_pk_fma_f32 v[18:19], v[0:1], v[24:25], v[18:19]
	v_pk_mul_f32 v[14:15], v[16:17], v[14:15]
	v_mul_f32_e32 v9, 0xbfb8aa3b, v18
	v_exp_f32_e32 v9, v9
	v_mul_f32_e32 v38, 0xbfb8aa3b, v19
	v_exp_f32_e32 v38, v38
	v_add_f32_e32 v9, 1.0, v9
	v_rcp_f32_e32 v16, v9
	v_add_f32_e32 v9, 1.0, v38
	v_pk_mul_f32 v[38:39], v[2:3], v[22:23]
	v_rcp_f32_e32 v17, v9
	v_pk_fma_f32 v[20:21], v[4:5], v[20:21], v[38:39]
	v_lshlrev_b32_e32 v38, 16, v52
	v_pk_fma_f32 v[20:21], v[6:7], v[24:25], v[20:21]
	v_and_b32_e32 v39, 0xffff0000, v52
	v_pk_fma_f32 v[20:21], v[0:1], v[38:39], v[20:21]
	v_pk_mul_f32 v[16:17], v[18:19], v[16:17]
	v_mul_f32_e32 v9, 0xbfb8aa3b, v20
	v_exp_f32_e32 v9, v9
	v_mul_f32_e32 v44, 0xbfb8aa3b, v21
	v_exp_f32_e32 v44, v44
	v_pk_mul_f32 v[56:57], v[2:3], v[38:39]
	v_add_f32_e32 v9, 1.0, v9
	v_rcp_f32_e32 v18, v9
	v_add_f32_e32 v9, 1.0, v44
	v_pk_mul_f32 v[44:45], v[2:3], v[24:25]
	v_rcp_f32_e32 v19, v9
	v_pk_fma_f32 v[22:23], v[4:5], v[22:23], v[44:45]
	v_lshlrev_b32_e32 v44, 16, v54
	v_pk_fma_f32 v[22:23], v[6:7], v[38:39], v[22:23]
	v_and_b32_e32 v45, 0xffff0000, v54
	v_pk_fma_f32 v[22:23], v[0:1], v[44:45], v[22:23]
	v_pk_fma_f32 v[24:25], v[4:5], v[24:25], v[56:57]
	v_mul_f32_e32 v9, 0xbfb8aa3b, v22
	v_exp_f32_e32 v9, v9
	v_mul_f32_e32 v46, 0xbfb8aa3b, v23
	v_exp_f32_e32 v46, v46
	v_pk_fma_f32 v[24:25], v[6:7], v[44:45], v[24:25]
	v_add_f32_e32 v9, 1.0, v9
	v_lshlrev_b32_e32 v56, 16, v60
	v_and_b32_e32 v57, 0xffff0000, v60
	v_pk_mul_f32 v[18:19], v[20:21], v[18:19]
	v_rcp_f32_e32 v20, v9
	v_add_f32_e32 v9, 1.0, v46
	v_pk_fma_f32 v[24:25], v[0:1], v[56:57], v[24:25]
	v_rcp_f32_e32 v21, v9
	v_mul_f32_e32 v9, 0xbfb8aa3b, v24
	v_exp_f32_e32 v9, v9
	v_mul_f32_e32 v46, 0xbfb8aa3b, v25
	v_exp_f32_e32 v46, v46
	v_pk_mul_f32 v[58:59], v[2:3], v[44:45]
	v_add_f32_e32 v9, 1.0, v9
	v_pk_fma_f32 v[38:39], v[4:5], v[38:39], v[58:59]
	v_lshlrev_b32_e32 v58, 16, v37
	v_pk_fma_f32 v[38:39], v[6:7], v[56:57], v[38:39]
	v_and_b32_e32 v59, 0xffff0000, v37
	v_pk_mul_f32 v[20:21], v[22:23], v[20:21]
	v_rcp_f32_e32 v22, v9
	v_add_f32_e32 v9, 1.0, v46
	v_pk_fma_f32 v[38:39], v[0:1], v[58:59], v[38:39]
	v_rcp_f32_e32 v23, v9
	v_mul_f32_e32 v9, 0xbfb8aa3b, v38
	v_exp_f32_e32 v9, v9
	v_mul_f32_e32 v37, 0xbfb8aa3b, v39
	v_exp_f32_e32 v37, v37
	v_pk_mul_f32 v[60:61], v[2:3], v[56:57]
	v_add_f32_e32 v9, 1.0, v9
	v_pk_fma_f32 v[44:45], v[4:5], v[44:45], v[60:61]
	v_lshlrev_b32_e32 v60, 16, v40
	v_pk_fma_f32 v[44:45], v[6:7], v[58:59], v[44:45]
	v_and_b32_e32 v61, 0xffff0000, v40
	v_pk_mul_f32 v[22:23], v[24:25], v[22:23]
	v_rcp_f32_e32 v24, v9
	v_add_f32_e32 v9, 1.0, v37
	v_pk_fma_f32 v[44:45], v[0:1], v[60:61], v[44:45]
	v_rcp_f32_e32 v25, v9
	v_mul_f32_e32 v9, 0xbfb8aa3b, v44
	v_exp_f32_e32 v9, v9
	v_mul_f32_e32 v37, 0xbfb8aa3b, v45
	v_exp_f32_e32 v37, v37
	v_pk_mul_f32 v[62:63], v[2:3], v[58:59]
	v_add_f32_e32 v9, 1.0, v9
	v_pk_fma_f32 v[56:57], v[4:5], v[56:57], v[62:63]
	v_lshlrev_b32_e32 v62, 16, v42
	v_pk_fma_f32 v[56:57], v[6:7], v[60:61], v[56:57]
	v_and_b32_e32 v63, 0xffff0000, v42
	v_pk_mul_f32 v[24:25], v[38:39], v[24:25]
	v_rcp_f32_e32 v38, v9
	v_add_f32_e32 v9, 1.0, v37
	v_pk_fma_f32 v[56:57], v[0:1], v[62:63], v[56:57]
	v_rcp_f32_e32 v39, v9
	v_mul_f32_e32 v9, 0xbfb8aa3b, v56
	v_exp_f32_e32 v9, v9
	v_mul_f32_e32 v37, 0xbfb8aa3b, v57
	v_exp_f32_e32 v37, v37
	v_pk_mul_f32 v[64:65], v[2:3], v[60:61]
	v_add_f32_e32 v9, 1.0, v9
	v_pk_fma_f32 v[58:59], v[4:5], v[58:59], v[64:65]
	v_lshlrev_b32_e32 v64, 16, v78
	v_pk_fma_f32 v[58:59], v[6:7], v[62:63], v[58:59]
	v_and_b32_e32 v65, 0xffff0000, v78
	v_pk_mul_f32 v[38:39], v[44:45], v[38:39]
	v_rcp_f32_e32 v44, v9
	v_add_f32_e32 v9, 1.0, v37
	v_pk_fma_f32 v[58:59], v[0:1], v[64:65], v[58:59]
	v_rcp_f32_e32 v45, v9
	v_mul_f32_e32 v9, 0xbfb8aa3b, v58
	v_exp_f32_e32 v9, v9
	v_mul_f32_e32 v37, 0xbfb8aa3b, v59
	v_exp_f32_e32 v37, v37
	v_pk_mul_f32 v[66:67], v[2:3], v[62:63]
; DI unsigned pk2(float lo, float hi) { f32x2 v = {lo, hi}; bf16x2_t b = __builtin_convertvector(v, bf16x2_t); return __builtin_bit_cast(unsigned, b); }
; #define MFMA16(a, b, c) __builtin_amdgcn_mfma_f32_16x16x32_bf16((a), (b), (c), 0, 0, 0)
; DI void gdn_prep_unit(const Params& p, int U, char* lds) {
;     ...
;       for (int ii = 0; ii < 16; ++ii) {
;         const int i = i0 + ii;
;         float a0 = y0[ii], a1 = y1[ii];
;         if (X < 2) { const float rn = rsqrtf(ssr[ii] + 1e-6f); a0 *= rn; a1 *= rn; }
;         *(unsigned*)(dst + i * QP + 2 * lane) = pk2(a0, a1);
;     ...
;   __syncthreads();
;   {
;     bf16x8 ka[4];
; #pragma unroll
;     for (int kk = 0; kk < 4; ++kk) ka[kk] = *(const bf16x8*)(k_s + (16 * wid + fr) * QP + kk * 32 + fq * 8);
; #pragma unroll
;     for (int ni = 0; ni < 4; ++ni) {
;       f32x4 dkk = {0.f, 0.f, 0.f, 0.f}, dqk = {0.f, 0.f, 0.f, 0.f};
;       const int i = 16 * ni + fr, jj0 = 16 * wid + 4 * fq;
;       if (ni >= wid) {
; #pragma unroll
;         for (int kk = 0; kk < 4; ++kk) {
;           const bf16x8 bk = *(const bf16x8*)(k_s + (16 * ni + fr) * QP + kk * 32 + fq * 8), bq = *(const bf16x8*)(q_s + (16 * ni + fr) * QP + kk * 32 + fq * 8);
;           dkk = MFMA16(ka[kk], bk, dkk); dqk = MFMA16(ka[kk], bq, dqk);
;         }
;       }
	v_add_f32_e32 v9, 1.0, v9
	v_pk_fma_f32 v[60:61], v[4:5], v[60:61], v[66:67]
	v_lshlrev_b32_e32 v66, 16, v79
	v_pk_fma_f32 v[60:61], v[6:7], v[64:65], v[60:61]
	v_and_b32_e32 v67, 0xffff0000, v79
	v_pk_mul_f32 v[44:45], v[56:57], v[44:45]
	v_rcp_f32_e32 v56, v9
	v_add_f32_e32 v9, 1.0, v37
	v_pk_fma_f32 v[60:61], v[0:1], v[66:67], v[60:61]
	v_rcp_f32_e32 v57, v9
	v_mul_f32_e32 v9, 0xbfb8aa3b, v60
	v_exp_f32_e32 v9, v9
	v_mul_f32_e32 v37, 0xbfb8aa3b, v61
	v_exp_f32_e32 v37, v37
	v_pk_mul_f32 v[68:69], v[2:3], v[64:65]
	v_add_f32_e32 v9, 1.0, v9
	v_pk_fma_f32 v[62:63], v[4:5], v[62:63], v[68:69]
	v_lshlrev_b32_e32 v68, 16, v80
	v_pk_fma_f32 v[62:63], v[6:7], v[66:67], v[62:63]
	v_and_b32_e32 v69, 0xffff0000, v80
	v_pk_mul_f32 v[56:57], v[58:59], v[56:57]
	v_rcp_f32_e32 v58, v9
	v_add_f32_e32 v9, 1.0, v37
	v_pk_fma_f32 v[62:63], v[0:1], v[68:69], v[62:63]
	v_rcp_f32_e32 v59, v9
	v_mul_f32_e32 v9, 0xbfb8aa3b, v62
	v_pk_mul_f32 v[70:71], v[2:3], v[66:67]
	v_exp_f32_e32 v9, v9
	v_mul_f32_e32 v37, 0xbfb8aa3b, v63
	v_pk_fma_f32 v[64:65], v[4:5], v[64:65], v[70:71]
	v_lshlrev_b32_e32 v70, 16, v81
	v_and_b32_e32 v71, 0xffff0000, v81
	v_exp_f32_e32 v37, v37
	v_pk_mul_f32 v[74:75], v[2:3], v[68:69]
	v_pk_mul_f32 v[2:3], v[2:3], v[70:71]
	v_pk_fma_f32 v[66:67], v[4:5], v[66:67], v[74:75]
	v_lshlrev_b32_e32 v74, 16, v82
	v_and_b32_e32 v75, 0xffff0000, v82
	v_pk_fma_f32 v[2:3], v[4:5], v[68:69], v[2:3]
	v_pk_fma_f32 v[64:65], v[6:7], v[68:69], v[64:65]
	v_pk_fma_f32 v[66:67], v[6:7], v[70:71], v[66:67]
	v_pk_fma_f32 v[2:3], v[6:7], v[74:75], v[2:3]
	v_lshlrev_b32_e32 v4, 16, v83
	v_and_b32_e32 v5, 0xffff0000, v83
	v_add_f32_e32 v9, 1.0, v9
	v_pk_fma_f32 v[64:65], v[0:1], v[70:71], v[64:65]
	v_pk_fma_f32 v[66:67], v[0:1], v[74:75], v[66:67]
	v_pk_fma_f32 v[0:1], v[0:1], v[4:5], v[2:3]
	v_pk_mul_f32 v[58:59], v[60:61], v[58:59]
	v_rcp_f32_e32 v60, v9
	v_add_f32_e32 v9, 1.0, v37
	v_mul_f32_e32 v37, 0xbfb8aa3b, v64
	v_mul_f32_e32 v2, 0xbfb8aa3b, v0
	v_mul_f32_e32 v3, 0xbfb8aa3b, v1
	v_exp_f32_e32 v37, v37
	v_mul_f32_e32 v40, 0xbfb8aa3b, v65
	v_exp_f32_e32 v2, v2
	v_exp_f32_e32 v3, v3
	v_exp_f32_e32 v40, v40
	v_rcp_f32_e32 v61, v9
	v_add_f32_e32 v9, 1.0, v37
	v_mul_f32_e32 v37, 0xbfb8aa3b, v66
	v_add_f32_e32 v2, 1.0, v2
	v_add_f32_e32 v3, 1.0, v3
	v_rcp_f32_e32 v72, v9
	v_add_f32_e32 v9, 1.0, v40
	v_exp_f32_e32 v37, v37
	v_mul_f32_e32 v40, 0xbfb8aa3b, v67
	v_rcp_f32_e32 v2, v2
	v_rcp_f32_e32 v3, v3
	v_exp_f32_e32 v40, v40
	v_rcp_f32_e32 v73, v9
	v_add_f32_e32 v9, 1.0, v37
	v_pk_mul_f32 v[0:1], v[0:1], v[2:3]
	v_cvt_pk_bf16_f32 v2, v10, v11
	v_rcp_f32_e32 v76, v9
	v_add_f32_e32 v9, 1.0, v40
	ds_write_b32 v8, v2 offset:34816
	v_cvt_pk_bf16_f32 v2, v12, v13
	v_cvt_pk_bf16_f32 v3, v14, v15
	v_add_u32_e32 v8, 0x8800, v36
	v_rcp_f32_e32 v77, v9
	ds_write2_b32 v8, v2, v3 offset1:68
	v_cvt_pk_bf16_f32 v2, v16, v17
	v_cvt_pk_bf16_f32 v3, v18, v19
	ds_write2_b32 v8, v2, v3 offset0:136 offset1:204
	v_cvt_pk_bf16_f32 v2, v20, v21
	v_cvt_pk_bf16_f32 v3, v22, v23
	v_add_u32_e32 v8, 0x8c00, v36
	ds_write2_b32 v8, v2, v3 offset0:16 offset1:84
	v_cvt_pk_bf16_f32 v2, v24, v25
	v_cvt_pk_bf16_f32 v3, v38, v39
	v_pk_mul_f32 v[4:5], v[62:63], v[60:61]
	ds_write2_b32 v8, v2, v3 offset0:152 offset1:220
	v_cvt_pk_bf16_f32 v2, v44, v45
	v_cvt_pk_bf16_f32 v3, v56, v57
	v_add_u32_e32 v8, 0x9000, v36
	v_pk_mul_f32 v[6:7], v[64:65], v[72:73]
	v_pk_mul_f32 v[60:61], v[66:67], v[76:77]
	ds_write2_b32 v8, v2, v3 offset0:32 offset1:100
	v_cvt_pk_bf16_f32 v2, v58, v59
	v_cvt_pk_bf16_f32 v3, v4, v5
	ds_write2_b32 v8, v2, v3 offset0:168 offset1:236
	v_cvt_pk_bf16_f32 v2, v6, v7
	v_cvt_pk_bf16_f32 v3, v60, v61
	v_add_u32_e32 v4, 0x9400, v36
	v_cvt_pk_bf16_f32 v0, v0, v1
	ds_write2_b32 v4, v2, v3 offset0:48 offset1:116
	ds_write_b32 v36, v0 offset:38624
	v_and_b32_e32 v0, 48, v178
	v_or_b32_e32 v46, v27, v55
	v_add_u32_e32 v42, v146, v0
	v_mad_u64_u32 v[0:1], s[0:1], v46, s18, v[42:43]
	s_waitcnt lgkmcnt(0)
	s_barrier
	ds_read_b128 v[12:15], v0 offset:17408
	ds_read_b128 v[8:11], v0 offset:17472
	ds_read_b128 v[4:7], v0 offset:17536
	ds_read_b128 v[0:3], v0 offset:17600
	v_mov_b32_e32 v16, 0
	v_mov_b32_e32 v18, 0
	v_mov_b32_e32 v19, 0
	v_mov_b32_e32 v20, 0
	v_mov_b32_e32 v21, 0
	v_mov_b32_e32 v22, 0
	v_mov_b32_e32 v23, 0
	v_mov_b32_e32 v24, 0
	v_mov_b32_e32 v25, 0
	s_and_saveexec_b64 s[0:1], vcc
	s_cbranch_execz .LBB0_1094
	v_mul_u32_u24_e32 v17, 0x88, v55
	v_lshl_add_u32 v17, v17, 1, v42
	ds_read_b128 v[18:21], v17 offset:17408
	ds_read_b128 v[22:25], v17 offset:17472
	ds_read_b128 v[36:39], v17
	ds_read_b128 v[56:59], v17 offset:64
	s_waitcnt lgkmcnt(3)
	v_mfma_f32_16x16x32_bf16 v[18:21], v[12:15], v[18:21], 0
	s_waitcnt lgkmcnt(1)
	v_mfma_f32_16x16x32_bf16 v[36:39], v[12:15], v[36:39], 0
	v_mfma_f32_16x16x32_bf16 v[18:21], v[8:11], v[22:25], v[18:21]
	s_waitcnt lgkmcnt(0)
	v_mfma_f32_16x16x32_bf16 v[22:25], v[8:11], v[56:59], v[36:39]
	s_nop 4
	ds_read_b128 v[36:39], v17 offset:17536
	ds_read_b128 v[56:59], v17 offset:17600
	s_waitcnt lgkmcnt(1)
	v_mfma_f32_16x16x32_bf16 v[18:21], v[4:7], v[36:39], v[18:21]
	ds_read_b128 v[36:39], v17 offset:128
	ds_read_b128 v[60:63], v17 offset:192
	s_waitcnt lgkmcnt(1)
	v_mfma_f32_16x16x32_bf16 v[36:39], v[4:7], v[36:39], v[22:25]
	v_mfma_f32_16x16x32_bf16 v[22:25], v[0:3], v[56:59], v[18:21]
	s_waitcnt lgkmcnt(0)
	v_mfma_f32_16x16x32_bf16 v[18:21], v[0:3], v[60:63], v[36:39]
